# P9 lru_scan2: gate-row loads are global (were FLAT), so the wait behind them is counted (vmcnt(32)) instead of a full drain; gate values waited at first use
# speedup vs baseline: 1.0083x; 1.0006x over previous
.LBB0_1466:
	v_add_u32_e32 v116, v171, v69
	v_add_u32_e32 v119, 0x800, v116
	ds_read2_b64 v[120:123], v119 offset0:224 offset1:240
	s_waitcnt lgkmcnt(0)
	v_pk_fma_f32 v[112:113], v[112:113], 0, v[114:115] op_sel_hi:[1,0,1]
	s_ashr_i32 s43, s42, 31
	v_pk_fma_f32 v[100:101], v[112:113], v[100:101], v[102:103]
	s_andn2_b64 vcc, exec, s[46:47]
	v_lshlrev_b32_e32 v114, 16, v122
	v_lshlrev_b32_e32 v124, 16, v123
	v_and_b32_e32 v115, 0xffff0000, v122
	v_add_f32_e32 v122, 0, v114
	v_mul_f32_e32 v114, 0x3fb8aa3b, v114
	v_exp_f32_e32 v117, v114
	v_mul_f32_e32 v114, 0x3fb8aa3b, v124
	v_exp_f32_e32 v118, v114
	v_and_b32_e32 v114, 0xffff0000, v123
	v_lshlrev_b32_e32 v123, 16, v120
	v_lshlrev_b32_e32 v125, 16, v121
	v_add_f32_e32 v128, v122, v123
	v_mul_f32_e32 v122, 0x3fb8aa3b, v123
	v_add_f32_e32 v124, 0, v124
	v_exp_f32_e32 v130, v122
	v_mul_f32_e32 v122, 0x3fb8aa3b, v125
	v_add_f32_e32 v129, v124, v125
	v_exp_f32_e32 v131, v122
	ds_read2_b64 v[122:125], v119 offset0:192 offset1:208
	v_fma_f32 v126, 0, v117, v115
	v_and_b32_e32 v120, 0xffff0000, v120
	v_fma_f32 v127, 0, v118, v114
	v_fmac_f32_e32 v120, v130, v126
	v_and_b32_e32 v121, 0xffff0000, v121
	s_waitcnt lgkmcnt(0)
	v_lshlrev_b32_e32 v126, 16, v124
	v_fmac_f32_e32 v121, v131, v127
	v_lshlrev_b32_e32 v127, 16, v125
	v_add_f32_e32 v128, v128, v126
	v_mul_f32_e32 v126, 0x3fb8aa3b, v126
	v_add_f32_e32 v129, v129, v127
	v_exp_f32_e32 v126, v126
	v_mul_f32_e32 v127, 0x3fb8aa3b, v127
	v_exp_f32_e32 v127, v127
	v_and_b32_e32 v130, 0xffff0000, v124
	v_fmac_f32_e32 v130, v126, v120
	v_and_b32_e32 v120, 0xffff0000, v125
	v_fmac_f32_e32 v120, v127, v121
	v_lshlrev_b32_e32 v121, 16, v122
	v_lshlrev_b32_e32 v124, 16, v123
	v_add_f32_e32 v128, v128, v121
	v_add_f32_e32 v129, v129, v124
	v_mul_f32_e32 v121, 0x3fb8aa3b, v121
	v_mul_f32_e32 v124, 0x3fb8aa3b, v124
	v_exp_f32_e32 v121, v121
	v_exp_f32_e32 v131, v124
	ds_read2_b64 v[124:127], v119 offset0:160 offset1:176
	v_and_b32_e32 v122, 0xffff0000, v122
	v_fmac_f32_e32 v122, v121, v130
	v_and_b32_e32 v121, 0xffff0000, v123
	v_fmac_f32_e32 v121, v131, v120
	s_waitcnt lgkmcnt(0)
	v_lshlrev_b32_e32 v120, 16, v126
	v_lshlrev_b32_e32 v123, 16, v127
	v_add_f32_e32 v128, v128, v120
	v_mul_f32_e32 v120, 0x3fb8aa3b, v120
	v_add_f32_e32 v129, v129, v123
	v_exp_f32_e32 v120, v120
	v_mul_f32_e32 v123, 0x3fb8aa3b, v123
	v_exp_f32_e32 v123, v123
	v_and_b32_e32 v126, 0xffff0000, v126
	v_fmac_f32_e32 v126, v120, v122
	v_and_b32_e32 v127, 0xffff0000, v127
	v_lshlrev_b32_e32 v120, 16, v124
	v_fmac_f32_e32 v127, v123, v121
	v_lshlrev_b32_e32 v121, 16, v125
	v_add_f32_e32 v128, v128, v120
	v_mul_f32_e32 v120, 0x3fb8aa3b, v120
	v_exp_f32_e32 v130, v120
	v_mul_f32_e32 v120, 0x3fb8aa3b, v121
	v_add_f32_e32 v129, v129, v121
	v_exp_f32_e32 v131, v120
	ds_read2_b64 v[120:123], v119 offset0:128 offset1:144
	v_and_b32_e32 v124, 0xffff0000, v124
	v_fmac_f32_e32 v124, v130, v126
	v_and_b32_e32 v125, 0xffff0000, v125
	v_fmac_f32_e32 v125, v131, v127
	s_waitcnt lgkmcnt(0)
	v_lshlrev_b32_e32 v126, 16, v122
	v_lshlrev_b32_e32 v127, 16, v123
	v_add_f32_e32 v128, v128, v126
	v_mul_f32_e32 v126, 0x3fb8aa3b, v126
	v_add_f32_e32 v129, v129, v127
	v_exp_f32_e32 v126, v126
	v_mul_f32_e32 v127, 0x3fb8aa3b, v127
	v_exp_f32_e32 v127, v127
	v_and_b32_e32 v130, 0xffff0000, v122
	v_fmac_f32_e32 v130, v126, v124
	v_and_b32_e32 v126, 0xffff0000, v123
	v_lshlrev_b32_e32 v122, 16, v120
	v_fmac_f32_e32 v126, v127, v125
	v_lshlrev_b32_e32 v123, 16, v121
	v_add_f32_e32 v127, v128, v122
	v_mul_f32_e32 v122, 0x3fb8aa3b, v122
	v_add_f32_e32 v128, v129, v123
	v_exp_f32_e32 v129, v122
	v_mul_f32_e32 v122, 0x3fb8aa3b, v123
	v_exp_f32_e32 v131, v122
	ds_read2_b64 v[122:125], v119 offset0:96 offset1:112
	v_and_b32_e32 v121, 0xffff0000, v121
	v_and_b32_e32 v120, 0xffff0000, v120
	v_fmac_f32_e32 v121, v131, v126
	v_fmac_f32_e32 v120, v129, v130
	s_waitcnt lgkmcnt(0)
	v_lshlrev_b32_e32 v126, 16, v124
	v_lshlrev_b32_e32 v129, 16, v125
	v_add_f32_e32 v127, v127, v126
	v_mul_f32_e32 v126, 0x3fb8aa3b, v126
	v_add_f32_e32 v128, v128, v129
	v_exp_f32_e32 v126, v126
	v_mul_f32_e32 v129, 0x3fb8aa3b, v129
	v_exp_f32_e32 v129, v129
	v_and_b32_e32 v130, 0xffff0000, v124
	v_fmac_f32_e32 v130, v126, v120
	v_and_b32_e32 v120, 0xffff0000, v125
	v_fmac_f32_e32 v120, v129, v121
	v_lshlrev_b32_e32 v121, 16, v122
	v_lshlrev_b32_e32 v124, 16, v123
	v_add_f32_e32 v129, v127, v121
	v_add_f32_e32 v128, v128, v124
	v_mul_f32_e32 v121, 0x3fb8aa3b, v121
	v_mul_f32_e32 v124, 0x3fb8aa3b, v124
	v_exp_f32_e32 v121, v121
	v_exp_f32_e32 v131, v124
	ds_read2_b64 v[124:127], v119 offset0:64 offset1:80
	v_and_b32_e32 v122, 0xffff0000, v122
	v_fmac_f32_e32 v122, v121, v130
	v_and_b32_e32 v121, 0xffff0000, v123
	v_fmac_f32_e32 v121, v131, v120
	s_waitcnt lgkmcnt(0)
	v_lshlrev_b32_e32 v120, 16, v126
	v_lshlrev_b32_e32 v123, 16, v127
	v_add_f32_e32 v129, v129, v120
	v_mul_f32_e32 v120, 0x3fb8aa3b, v120
	v_add_f32_e32 v128, v128, v123
	v_exp_f32_e32 v120, v120
	v_mul_f32_e32 v123, 0x3fb8aa3b, v123
	v_exp_f32_e32 v123, v123
	v_and_b32_e32 v126, 0xffff0000, v126
	v_fmac_f32_e32 v126, v120, v122
	v_and_b32_e32 v127, 0xffff0000, v127
	v_lshlrev_b32_e32 v120, 16, v124
	v_fmac_f32_e32 v127, v123, v121
	v_lshlrev_b32_e32 v121, 16, v125
	v_add_f32_e32 v129, v129, v120
	v_mul_f32_e32 v120, 0x3fb8aa3b, v120
	v_exp_f32_e32 v130, v120
	v_mul_f32_e32 v120, 0x3fb8aa3b, v121
	v_add_f32_e32 v128, v128, v121
	v_exp_f32_e32 v131, v120
	ds_read2_b64 v[120:123], v119 offset0:32 offset1:48
	v_and_b32_e32 v124, 0xffff0000, v124
	v_fmac_f32_e32 v124, v130, v126
	v_and_b32_e32 v125, 0xffff0000, v125
	v_fmac_f32_e32 v125, v131, v127
	s_waitcnt lgkmcnt(0)
	v_lshlrev_b32_e32 v126, 16, v122
	v_lshlrev_b32_e32 v127, 16, v123
	v_add_f32_e32 v129, v129, v126
	v_mul_f32_e32 v126, 0x3fb8aa3b, v126
	v_add_f32_e32 v128, v128, v127
	v_exp_f32_e32 v126, v126
	v_mul_f32_e32 v127, 0x3fb8aa3b, v127
	v_exp_f32_e32 v127, v127
	v_and_b32_e32 v130, 0xffff0000, v122
	v_fmac_f32_e32 v130, v126, v124
	v_and_b32_e32 v126, 0xffff0000, v123
	v_lshlrev_b32_e32 v122, 16, v120
	v_fmac_f32_e32 v126, v127, v125
	v_lshlrev_b32_e32 v123, 16, v121
	v_add_f32_e32 v127, v129, v122
	v_mul_f32_e32 v122, 0x3fb8aa3b, v122
	v_exp_f32_e32 v129, v122
	v_mul_f32_e32 v122, 0x3fb8aa3b, v123
	v_add_f32_e32 v128, v128, v123
	v_exp_f32_e32 v131, v122
	ds_read2_b64 v[122:125], v119 offset1:16
	v_and_b32_e32 v119, 0xffff0000, v120
	v_and_b32_e32 v120, 0xffff0000, v121
	v_fmac_f32_e32 v120, v131, v126
	v_fmac_f32_e32 v119, v129, v130
	s_waitcnt lgkmcnt(0)
	v_lshlrev_b32_e32 v121, 16, v124
	v_lshlrev_b32_e32 v126, 16, v125
	v_add_f32_e32 v127, v127, v121
	v_mul_f32_e32 v121, 0x3fb8aa3b, v121
	v_add_f32_e32 v128, v128, v126
	v_exp_f32_e32 v121, v121
	v_mul_f32_e32 v126, 0x3fb8aa3b, v126
	v_exp_f32_e32 v126, v126
	v_and_b32_e32 v129, 0xffff0000, v124
	v_fmac_f32_e32 v129, v121, v119
	v_and_b32_e32 v119, 0xffff0000, v125
	v_fmac_f32_e32 v119, v126, v120
	v_lshlrev_b32_e32 v120, 16, v122
	v_lshlrev_b32_e32 v121, 16, v123
	v_add_f32_e32 v130, v127, v120
	v_mul_f32_e32 v120, 0x3fb8aa3b, v120
	v_add_f32_e32 v128, v128, v121
	v_exp_f32_e32 v120, v120
	v_mul_f32_e32 v121, 0x3fb8aa3b, v121
	ds_read2_b64 v[124:127], v116 offset0:224 offset1:240
	v_exp_f32_e32 v121, v121
	v_and_b32_e32 v122, 0xffff0000, v122
	v_fmac_f32_e32 v122, v120, v129
	v_and_b32_e32 v120, 0xffff0000, v123
	v_fmac_f32_e32 v120, v121, v119
	s_waitcnt lgkmcnt(0)
	v_lshlrev_b32_e32 v119, 16, v126
	v_lshlrev_b32_e32 v121, 16, v127
	v_add_f32_e32 v123, v130, v119
	v_mul_f32_e32 v119, 0x3fb8aa3b, v119
	v_add_f32_e32 v128, v128, v121
	v_exp_f32_e32 v119, v119
	v_mul_f32_e32 v121, 0x3fb8aa3b, v121
	v_exp_f32_e32 v121, v121
	v_and_b32_e32 v126, 0xffff0000, v126
	v_fmac_f32_e32 v126, v119, v122
	v_and_b32_e32 v119, 0xffff0000, v127
	v_fmac_f32_e32 v119, v121, v120
	v_lshlrev_b32_e32 v120, 16, v124
	v_lshlrev_b32_e32 v121, 16, v125
	v_add_f32_e32 v127, v123, v120
	v_mul_f32_e32 v120, 0x3fb8aa3b, v120
	v_exp_f32_e32 v129, v120
	v_mul_f32_e32 v120, 0x3fb8aa3b, v121
	v_add_f32_e32 v128, v128, v121
	v_exp_f32_e32 v130, v120
	ds_read2_b64 v[120:123], v116 offset0:192 offset1:208
	v_and_b32_e32 v125, 0xffff0000, v125
	v_and_b32_e32 v124, 0xffff0000, v124
	v_fmac_f32_e32 v125, v130, v119
	v_fmac_f32_e32 v124, v129, v126
	s_waitcnt lgkmcnt(0)
	v_lshlrev_b32_e32 v119, 16, v122
	v_lshlrev_b32_e32 v126, 16, v123
	v_add_f32_e32 v127, v127, v119
	v_mul_f32_e32 v119, 0x3fb8aa3b, v119
	v_add_f32_e32 v128, v128, v126
	v_exp_f32_e32 v119, v119
	v_mul_f32_e32 v126, 0x3fb8aa3b, v126
	v_exp_f32_e32 v126, v126
	v_and_b32_e32 v129, 0xffff0000, v122
	v_fmac_f32_e32 v129, v119, v124
	v_and_b32_e32 v119, 0xffff0000, v123
	v_lshlrev_b32_e32 v122, 16, v120
	v_fmac_f32_e32 v119, v126, v125
	v_lshlrev_b32_e32 v123, 16, v121
	v_add_f32_e32 v126, v127, v122
	v_mul_f32_e32 v122, 0x3fb8aa3b, v122
	v_add_f32_e32 v127, v128, v123
	v_exp_f32_e32 v128, v122
	v_mul_f32_e32 v122, 0x3fb8aa3b, v123
	v_exp_f32_e32 v130, v122
	ds_read2_b64 v[122:125], v116 offset0:160 offset1:176
	v_and_b32_e32 v121, 0xffff0000, v121
	v_and_b32_e32 v120, 0xffff0000, v120
	v_fmac_f32_e32 v121, v130, v119
	v_fmac_f32_e32 v120, v128, v129
	s_waitcnt lgkmcnt(0)
	v_lshlrev_b32_e32 v119, 16, v124
	v_lshlrev_b32_e32 v128, 16, v125
	v_add_f32_e32 v126, v126, v119
	v_mul_f32_e32 v119, 0x3fb8aa3b, v119
	v_add_f32_e32 v127, v127, v128
	v_exp_f32_e32 v119, v119
	v_mul_f32_e32 v128, 0x3fb8aa3b, v128
	v_exp_f32_e32 v128, v128
	v_and_b32_e32 v129, 0xffff0000, v124
	v_fmac_f32_e32 v129, v119, v120
	v_and_b32_e32 v119, 0xffff0000, v125
	v_lshlrev_b32_e32 v120, 16, v122
	v_fmac_f32_e32 v119, v128, v121
	v_lshlrev_b32_e32 v121, 16, v123
	v_add_f32_e32 v128, v126, v120
	v_mul_f32_e32 v120, 0x3fb8aa3b, v120
	v_add_f32_e32 v130, v127, v121
	v_exp_f32_e32 v120, v120
	v_mul_f32_e32 v121, 0x3fb8aa3b, v121
	ds_read2_b64 v[124:127], v116 offset0:128 offset1:144
	v_exp_f32_e32 v121, v121
	v_and_b32_e32 v122, 0xffff0000, v122
	v_fmac_f32_e32 v122, v120, v129
	v_and_b32_e32 v120, 0xffff0000, v123
	v_fmac_f32_e32 v120, v121, v119
	s_waitcnt lgkmcnt(0)
	v_lshlrev_b32_e32 v119, 16, v126
	v_lshlrev_b32_e32 v121, 16, v127
	v_add_f32_e32 v123, v128, v119
	v_mul_f32_e32 v119, 0x3fb8aa3b, v119
	v_add_f32_e32 v128, v130, v121
	v_exp_f32_e32 v119, v119
	v_mul_f32_e32 v121, 0x3fb8aa3b, v121
	v_exp_f32_e32 v121, v121
	v_and_b32_e32 v126, 0xffff0000, v126
	v_fmac_f32_e32 v126, v119, v122
	v_and_b32_e32 v119, 0xffff0000, v127
	v_fmac_f32_e32 v119, v121, v120
	v_lshlrev_b32_e32 v120, 16, v124
	v_lshlrev_b32_e32 v121, 16, v125
	v_add_f32_e32 v127, v123, v120
	v_mul_f32_e32 v120, 0x3fb8aa3b, v120
	v_exp_f32_e32 v129, v120
	v_mul_f32_e32 v120, 0x3fb8aa3b, v121
	v_add_f32_e32 v128, v128, v121
	v_exp_f32_e32 v130, v120
	ds_read2_b64 v[120:123], v116 offset0:96 offset1:112
	v_and_b32_e32 v125, 0xffff0000, v125
	v_and_b32_e32 v124, 0xffff0000, v124
	v_fmac_f32_e32 v125, v130, v119
	v_fmac_f32_e32 v124, v129, v126
	s_waitcnt lgkmcnt(0)
	v_lshlrev_b32_e32 v119, 16, v122
	v_lshlrev_b32_e32 v126, 16, v123
	v_add_f32_e32 v127, v127, v119
	v_mul_f32_e32 v119, 0x3fb8aa3b, v119
	v_add_f32_e32 v128, v128, v126
	v_exp_f32_e32 v119, v119
	v_mul_f32_e32 v126, 0x3fb8aa3b, v126
	v_exp_f32_e32 v126, v126
	v_and_b32_e32 v129, 0xffff0000, v122
	v_fmac_f32_e32 v129, v119, v124
	v_and_b32_e32 v119, 0xffff0000, v123
	v_lshlrev_b32_e32 v122, 16, v120
	v_fmac_f32_e32 v119, v126, v125
	v_lshlrev_b32_e32 v123, 16, v121
	v_add_f32_e32 v126, v127, v122
	v_mul_f32_e32 v122, 0x3fb8aa3b, v122
	v_add_f32_e32 v127, v128, v123
	v_exp_f32_e32 v128, v122
	v_mul_f32_e32 v122, 0x3fb8aa3b, v123
	v_exp_f32_e32 v130, v122
	ds_read2_b64 v[122:125], v116 offset0:64 offset1:80
	v_and_b32_e32 v121, 0xffff0000, v121
	v_and_b32_e32 v120, 0xffff0000, v120
	v_fmac_f32_e32 v121, v130, v119
	v_fmac_f32_e32 v120, v128, v129
	s_waitcnt lgkmcnt(0)
	v_lshlrev_b32_e32 v119, 16, v124
	v_lshlrev_b32_e32 v128, 16, v125
	v_add_f32_e32 v126, v126, v119
	v_mul_f32_e32 v119, 0x3fb8aa3b, v119
	v_add_f32_e32 v127, v127, v128
	v_exp_f32_e32 v119, v119
	v_mul_f32_e32 v128, 0x3fb8aa3b, v128
	v_exp_f32_e32 v128, v128
	v_and_b32_e32 v129, 0xffff0000, v124
	v_fmac_f32_e32 v129, v119, v120
	v_and_b32_e32 v119, 0xffff0000, v125
	v_lshlrev_b32_e32 v120, 16, v122
	v_fmac_f32_e32 v119, v128, v121
	v_lshlrev_b32_e32 v121, 16, v123
	v_add_f32_e32 v128, v126, v120
	v_mul_f32_e32 v120, 0x3fb8aa3b, v120
	v_add_f32_e32 v130, v127, v121
	v_exp_f32_e32 v120, v120
	v_mul_f32_e32 v121, 0x3fb8aa3b, v121
	ds_read2_b64 v[124:127], v116 offset0:32 offset1:48
	v_exp_f32_e32 v121, v121
	v_and_b32_e32 v122, 0xffff0000, v122
	v_fmac_f32_e32 v122, v120, v129
	v_and_b32_e32 v120, 0xffff0000, v123
	v_fmac_f32_e32 v120, v121, v119
	s_waitcnt lgkmcnt(0)
	v_lshlrev_b32_e32 v119, 16, v126
	v_lshlrev_b32_e32 v121, 16, v127
	v_add_f32_e32 v123, v128, v119
	v_mul_f32_e32 v119, 0x3fb8aa3b, v119
	v_add_f32_e32 v128, v130, v121
	v_exp_f32_e32 v119, v119
	v_mul_f32_e32 v121, 0x3fb8aa3b, v121
	v_exp_f32_e32 v121, v121
	v_and_b32_e32 v126, 0xffff0000, v126
	v_fmac_f32_e32 v126, v119, v122
	v_and_b32_e32 v119, 0xffff0000, v127
	v_fmac_f32_e32 v119, v121, v120
	v_lshlrev_b32_e32 v120, 16, v124
	v_lshlrev_b32_e32 v121, 16, v125
	v_add_f32_e32 v127, v123, v120
	v_mul_f32_e32 v120, 0x3fb8aa3b, v120
	v_exp_f32_e32 v129, v120
	v_mul_f32_e32 v120, 0x3fb8aa3b, v121
	v_add_f32_e32 v128, v128, v121
	v_exp_f32_e32 v130, v120
	ds_read2_b64 v[120:123], v116 offset1:16
	v_and_b32_e32 v125, 0xffff0000, v125
	v_and_b32_e32 v124, 0xffff0000, v124
	v_fmac_f32_e32 v125, v130, v119
	v_fmac_f32_e32 v124, v129, v126
	s_waitcnt lgkmcnt(0)
	v_lshlrev_b32_e32 v119, 16, v122
	v_lshlrev_b32_e32 v126, 16, v123
	v_add_f32_e32 v127, v127, v119
	v_mul_f32_e32 v119, 0x3fb8aa3b, v119
	v_add_f32_e32 v128, v128, v126
	v_exp_f32_e32 v119, v119
	v_mul_f32_e32 v126, 0x3fb8aa3b, v126
	v_exp_f32_e32 v126, v126
	v_and_b32_e32 v122, 0xffff0000, v122
	v_fmac_f32_e32 v122, v119, v124
	v_and_b32_e32 v119, 0xffff0000, v123
	v_lshlrev_b32_e32 v123, 16, v120
	v_fmac_f32_e32 v119, v126, v125
	v_mul_f32_e32 v125, 0x3fb8aa3b, v123
	v_exp_f32_e32 v125, v125
	v_lshlrev_b32_e32 v124, 16, v121
	v_add_f32_e32 v123, v127, v123
	v_and_b32_e32 v120, 0xffff0000, v120
	v_fmac_f32_e32 v120, v125, v122
	v_mul_f32_e32 v122, 0x3fb8aa3b, v124
	v_mul_f32_e32 v123, 0x3fb8aa3b, v123
	v_exp_f32_e32 v122, v122
	v_exp_f32_e32 v123, v123
	v_and_b32_e32 v121, 0xffff0000, v121
	ds_bpermute_b32 v125, v168, v120
	v_fmac_f32_e32 v121, v122, v119
	ds_bpermute_b32 v119, v168, v123
	ds_bpermute_b32 v102, v167, v123
	ds_bpermute_b32 v103, v167, v120
	v_pk_fma_f32 v[100:101], v[100:101], v[104:105], v[106:107]
	ds_bpermute_b32 v107, v166, v120
	v_pk_fma_f32 v[100:101], v[100:101], v[108:109], v[110:111]
	v_add_f32_e32 v126, v128, v124
	s_waitcnt lgkmcnt(3)
	v_fmac_f32_e32 v125, v100, v119
	v_cndmask_b32_e64 v100, v125, v100, s[6:7]
	s_waitcnt lgkmcnt(1)
	v_fmac_f32_e32 v103, v100, v102
	ds_bpermute_b32 v102, v166, v123
	v_cndmask_b32_e64 v100, v100, v103, s[8:9]
	v_mul_f32_e32 v124, 0x3fb8aa3b, v126
	v_exp_f32_e32 v124, v124
	ds_bpermute_b32 v126, v168, v121
	s_waitcnt lgkmcnt(1)
	v_fmac_f32_e32 v107, v100, v102
	s_waitcnt vmcnt(16)
	v_lshlrev_b32_e32 v102, 16, v236
	v_mul_f32_e32 v103, 0x3d372713, v102
	v_mul_f32_e32 v103, v103, v102
	v_fma_f32 v103, v103, v102, v102
	v_mul_f32_e32 v103, 0x3f4c422a, v103
	ds_bpermute_b32 v122, v168, v124
	v_add_f32_e32 v103, v103, v103
	v_mul_f32_e32 v103, 0x3fb8aa3b, v103
	ds_bpermute_b32 v104, v167, v124
	ds_bpermute_b32 v105, v167, v121
	v_exp_f32_e32 v103, v103
	s_waitcnt lgkmcnt(2)
	v_fmac_f32_e32 v126, v101, v122
	v_cndmask_b32_e64 v100, v100, v107, s[0:1]
	v_cndmask_b32_e64 v101, v126, v101, s[6:7]
	v_fmac_f32_e32 v115, v117, v100
	v_add_f32_e32 v100, 1.0, v103
	v_and_b32_e32 v103, 0xffff0000, v236
	s_waitcnt lgkmcnt(0)
	v_fmac_f32_e32 v105, v101, v104
	v_mul_f32_e32 v104, 0x3d372713, v103
	v_mul_f32_e32 v104, v104, v103
	v_fma_f32 v104, v104, v103, v103
	v_mul_f32_e32 v104, 0x3f4c422a, v104
	v_rcp_f32_e32 v100, v100
	v_add_f32_e32 v104, v104, v104
	v_mul_f32_e32 v104, 0x3fb8aa3b, v104
	v_exp_f32_e32 v104, v104
	ds_bpermute_b32 v106, v166, v124
	ds_bpermute_b32 v108, v166, v121
	v_fma_f32 v100, v100, -2.0, 1.0
	v_mul_f32_e32 v102, 0.5, v102
	v_add_f32_e32 v100, 1.0, v100
	v_mul_f32_e32 v100, v102, v100
	v_add_f32_e32 v102, 1.0, v104
	v_cndmask_b32_e64 v101, v101, v105, s[8:9]
	v_rcp_f32_e32 v102, v102
	s_waitcnt lgkmcnt(0)
	v_fmac_f32_e32 v108, v101, v106
	v_cndmask_b32_e64 v101, v101, v108, s[0:1]
	v_fmac_f32_e32 v114, v118, v101
	v_lshlrev_b32_e32 v101, 16, v233
	v_add_f32_e32 v101, v115, v101
	v_fma_f32 v102, v102, -2.0, 1.0
	v_mul_f32_e32 v100, v100, v101
	v_and_b32_e32 v101, 0xffff0000, v233
	v_mul_f32_e32 v103, 0.5, v103
	v_add_f32_e32 v102, 1.0, v102
	v_add_f32_e32 v101, v114, v101
	v_mul_f32_e32 v102, v103, v102
	v_mul_f32_e32 v101, v102, v101
	v_cvt_pk_bf16_f32 v102, v100, v101
	ds_read_b64 v[100:101], v116 offset:3840
	ds_write_b32 v190, v102 offset:3968
	s_add_i32 s34, s34, s35
	s_waitcnt lgkmcnt(1)
	v_lshlrev_b32_e32 v103, 16, v100
	v_mul_f32_e32 v103, 0x3fb8aa3b, v103
	v_exp_f32_e32 v103, v103
	v_and_b32_e32 v102, 0xffff0000, v100
	v_lshlrev_b32_e32 v100, 16, v101
	v_and_b32_e32 v105, 0xffff0000, v101
	v_fmac_f32_e32 v102, v115, v103
	v_lshlrev_b32_e32 v103, 16, v235
	v_mul_f32_e32 v104, 0x3d372713, v103
	v_mul_f32_e32 v104, v104, v103
	v_fma_f32 v104, v104, v103, v103
	v_mul_f32_e32 v104, 0x3f4c422a, v104
	v_add_f32_e32 v104, v104, v104
	v_mul_f32_e32 v104, 0x3fb8aa3b, v104
	v_exp_f32_e32 v104, v104
	v_mul_f32_e32 v100, 0x3fb8aa3b, v100
	v_mul_f32_e32 v103, 0.5, v103
	v_exp_f32_e32 v100, v100
	v_add_f32_e32 v101, 1.0, v104
	v_and_b32_e32 v104, 0xffff0000, v235
	v_mul_f32_e32 v106, 0x3d372713, v104
	v_mul_f32_e32 v106, v106, v104
	v_fma_f32 v106, v106, v104, v104
	v_mul_f32_e32 v106, 0x3f4c422a, v106
	v_rcp_f32_e32 v101, v101
	v_add_f32_e32 v106, v106, v106
	v_mul_f32_e32 v106, 0x3fb8aa3b, v106
	v_exp_f32_e32 v106, v106
	v_fma_f32 v101, v101, -2.0, 1.0
	v_add_f32_e32 v101, 1.0, v101
	v_mul_f32_e32 v101, v103, v101
	v_add_f32_e32 v103, 1.0, v106
	v_rcp_f32_e32 v103, v103
	v_fmac_f32_e32 v105, v114, v100
	v_lshlrev_b32_e32 v100, 16, v231
	v_add_f32_e32 v100, v102, v100
	v_fma_f32 v103, v103, -2.0, 1.0
	v_mul_f32_e32 v100, v101, v100
	v_and_b32_e32 v101, 0xffff0000, v231
	v_mul_f32_e32 v104, 0.5, v104
	v_add_f32_e32 v103, 1.0, v103
	v_add_f32_e32 v101, v105, v101
	v_mul_f32_e32 v103, v104, v103
	v_mul_f32_e32 v101, v103, v101
	v_cvt_pk_bf16_f32 v103, v100, v101
	ds_read_b64 v[100:101], v116 offset:3712
	ds_write_b32 v190, v103 offset:3840
	s_waitcnt lgkmcnt(1)
	v_lshlrev_b32_e32 v104, 16, v100
	v_mul_f32_e32 v104, 0x3fb8aa3b, v104
	v_exp_f32_e32 v104, v104
	v_and_b32_e32 v103, 0xffff0000, v100
	v_lshlrev_b32_e32 v100, 16, v101
	v_mul_f32_e32 v100, 0x3fb8aa3b, v100
	v_fmac_f32_e32 v103, v102, v104
	v_lshlrev_b32_e32 v102, 16, v234
	v_mul_f32_e32 v104, 0x3d372713, v102
	v_mul_f32_e32 v104, v104, v102
	v_fma_f32 v104, v104, v102, v102
	v_mul_f32_e32 v104, 0x3f4c422a, v104
	v_add_f32_e32 v104, v104, v104
	v_mul_f32_e32 v104, 0x3fb8aa3b, v104
	v_exp_f32_e32 v104, v104
	v_exp_f32_e32 v100, v100
	v_and_b32_e32 v106, 0xffff0000, v101
	v_mul_f32_e32 v102, 0.5, v102
	v_add_f32_e32 v101, 1.0, v104
	v_and_b32_e32 v104, 0xffff0000, v234
	v_fmac_f32_e32 v106, v105, v100
	v_mul_f32_e32 v105, 0x3d372713, v104
	v_mul_f32_e32 v105, v105, v104
	v_fma_f32 v105, v105, v104, v104
	v_mul_f32_e32 v105, 0x3f4c422a, v105
	v_rcp_f32_e32 v101, v101
	v_add_f32_e32 v105, v105, v105
	v_mul_f32_e32 v105, 0x3fb8aa3b, v105
	v_exp_f32_e32 v105, v105
	v_fma_f32 v101, v101, -2.0, 1.0
	v_add_f32_e32 v101, 1.0, v101
	v_mul_f32_e32 v101, v102, v101
	v_add_f32_e32 v102, 1.0, v105
	v_rcp_f32_e32 v102, v102
	v_lshlrev_b32_e32 v100, 16, v229
	v_add_f32_e32 v100, v103, v100
	v_mul_f32_e32 v100, v101, v100
	v_fma_f32 v102, v102, -2.0, 1.0
	v_and_b32_e32 v101, 0xffff0000, v229
	v_mul_f32_e32 v104, 0.5, v104
	v_add_f32_e32 v102, 1.0, v102
	v_add_f32_e32 v101, v106, v101
	v_mul_f32_e32 v102, v104, v102
	v_mul_f32_e32 v101, v102, v101
	v_cvt_pk_bf16_f32 v102, v100, v101
	ds_read_b64 v[100:101], v116 offset:3584
	ds_write_b32 v190, v102 offset:3712
	s_waitcnt lgkmcnt(1)
	v_lshlrev_b32_e32 v104, 16, v100
	v_mul_f32_e32 v104, 0x3fb8aa3b, v104
	v_exp_f32_e32 v104, v104
	v_and_b32_e32 v102, 0xffff0000, v100
	v_lshlrev_b32_e32 v100, 16, v101
	v_mul_f32_e32 v100, 0x3fb8aa3b, v100
	v_fmac_f32_e32 v102, v103, v104
	v_lshlrev_b32_e32 v103, 16, v232
	v_mul_f32_e32 v104, 0x3d372713, v103
	v_mul_f32_e32 v104, v104, v103
	v_fma_f32 v104, v104, v103, v103
	v_mul_f32_e32 v104, 0x3f4c422a, v104
	v_add_f32_e32 v104, v104, v104
	v_mul_f32_e32 v104, 0x3fb8aa3b, v104
	v_exp_f32_e32 v104, v104
	v_exp_f32_e32 v100, v100
	v_and_b32_e32 v105, 0xffff0000, v101
	v_mul_f32_e32 v103, 0.5, v103
	v_add_f32_e32 v101, 1.0, v104
	v_and_b32_e32 v104, 0xffff0000, v232
	v_fmac_f32_e32 v105, v106, v100
	v_mul_f32_e32 v106, 0x3d372713, v104
	v_mul_f32_e32 v106, v106, v104
	v_fma_f32 v106, v106, v104, v104
	v_mul_f32_e32 v106, 0x3f4c422a, v106
	v_rcp_f32_e32 v101, v101
	v_add_f32_e32 v106, v106, v106
	v_mul_f32_e32 v106, 0x3fb8aa3b, v106
	v_exp_f32_e32 v106, v106
	v_fma_f32 v101, v101, -2.0, 1.0
	v_add_f32_e32 v101, 1.0, v101
	v_mul_f32_e32 v101, v103, v101
	v_add_f32_e32 v103, 1.0, v106
	v_rcp_f32_e32 v103, v103
	v_lshlrev_b32_e32 v100, 16, v227
	v_add_f32_e32 v100, v102, v100
	v_mul_f32_e32 v100, v101, v100
	v_fma_f32 v103, v103, -2.0, 1.0
	v_and_b32_e32 v101, 0xffff0000, v227
	v_mul_f32_e32 v104, 0.5, v104
	v_add_f32_e32 v103, 1.0, v103
	v_add_f32_e32 v101, v105, v101
	v_mul_f32_e32 v103, v104, v103
	v_mul_f32_e32 v101, v103, v101
	v_cvt_pk_bf16_f32 v103, v100, v101
	ds_read_b64 v[100:101], v116 offset:3456
	ds_write_b32 v190, v103 offset:3584
	s_waitcnt lgkmcnt(1)
	v_lshlrev_b32_e32 v104, 16, v100
	v_mul_f32_e32 v104, 0x3fb8aa3b, v104
	v_exp_f32_e32 v104, v104
	v_and_b32_e32 v103, 0xffff0000, v100
	v_lshlrev_b32_e32 v100, 16, v101
	v_mul_f32_e32 v100, 0x3fb8aa3b, v100
	v_fmac_f32_e32 v103, v102, v104
	v_lshlrev_b32_e32 v102, 16, v230
	v_mul_f32_e32 v104, 0x3d372713, v102
	v_mul_f32_e32 v104, v104, v102
	v_fma_f32 v104, v104, v102, v102
	v_mul_f32_e32 v104, 0x3f4c422a, v104
	v_add_f32_e32 v104, v104, v104
	v_mul_f32_e32 v104, 0x3fb8aa3b, v104
	v_exp_f32_e32 v104, v104
	v_exp_f32_e32 v100, v100
	v_and_b32_e32 v106, 0xffff0000, v101
	v_mul_f32_e32 v102, 0.5, v102
	v_add_f32_e32 v101, 1.0, v104
	v_and_b32_e32 v104, 0xffff0000, v230
	v_fmac_f32_e32 v106, v105, v100
	v_mul_f32_e32 v105, 0x3d372713, v104
	v_mul_f32_e32 v105, v105, v104
	v_fma_f32 v105, v105, v104, v104
	v_mul_f32_e32 v105, 0x3f4c422a, v105
	v_rcp_f32_e32 v101, v101
	v_add_f32_e32 v105, v105, v105
	v_mul_f32_e32 v105, 0x3fb8aa3b, v105
	v_exp_f32_e32 v105, v105
	v_fma_f32 v101, v101, -2.0, 1.0
	v_add_f32_e32 v101, 1.0, v101
	v_mul_f32_e32 v101, v102, v101
	v_add_f32_e32 v102, 1.0, v105
	v_rcp_f32_e32 v102, v102
	v_lshlrev_b32_e32 v100, 16, v225
	v_add_f32_e32 v100, v103, v100
	v_mul_f32_e32 v100, v101, v100
	v_fma_f32 v102, v102, -2.0, 1.0
	v_and_b32_e32 v101, 0xffff0000, v225
	v_mul_f32_e32 v104, 0.5, v104
	v_add_f32_e32 v102, 1.0, v102
	v_add_f32_e32 v101, v106, v101
	v_mul_f32_e32 v102, v104, v102
	v_mul_f32_e32 v101, v102, v101
	v_cvt_pk_bf16_f32 v102, v100, v101
	ds_read_b64 v[100:101], v116 offset:3328
	ds_write_b32 v190, v102 offset:3456
	s_waitcnt lgkmcnt(1)
	v_lshlrev_b32_e32 v104, 16, v100
	v_mul_f32_e32 v104, 0x3fb8aa3b, v104
	v_exp_f32_e32 v104, v104
	v_and_b32_e32 v102, 0xffff0000, v100
	v_lshlrev_b32_e32 v100, 16, v101
	v_mul_f32_e32 v100, 0x3fb8aa3b, v100
	v_fmac_f32_e32 v102, v103, v104
	v_lshlrev_b32_e32 v103, 16, v228
	v_mul_f32_e32 v104, 0x3d372713, v103
	v_mul_f32_e32 v104, v104, v103
	v_fma_f32 v104, v104, v103, v103
	v_mul_f32_e32 v104, 0x3f4c422a, v104
	v_add_f32_e32 v104, v104, v104
	v_mul_f32_e32 v104, 0x3fb8aa3b, v104
	v_exp_f32_e32 v104, v104
	v_exp_f32_e32 v100, v100
	v_and_b32_e32 v105, 0xffff0000, v101
	v_mul_f32_e32 v103, 0.5, v103
	v_add_f32_e32 v101, 1.0, v104
	v_and_b32_e32 v104, 0xffff0000, v228
	v_fmac_f32_e32 v105, v106, v100
	v_mul_f32_e32 v106, 0x3d372713, v104
	v_mul_f32_e32 v106, v106, v104
	v_fma_f32 v106, v106, v104, v104
	v_mul_f32_e32 v106, 0x3f4c422a, v106
	v_rcp_f32_e32 v101, v101
	v_add_f32_e32 v106, v106, v106
	v_mul_f32_e32 v106, 0x3fb8aa3b, v106
	v_exp_f32_e32 v106, v106
	v_fma_f32 v101, v101, -2.0, 1.0
	v_add_f32_e32 v101, 1.0, v101
	v_mul_f32_e32 v101, v103, v101
	v_add_f32_e32 v103, 1.0, v106
	v_rcp_f32_e32 v103, v103
	v_lshlrev_b32_e32 v100, 16, v222
	v_add_f32_e32 v100, v102, v100
	v_mul_f32_e32 v100, v101, v100
	v_fma_f32 v103, v103, -2.0, 1.0
	v_and_b32_e32 v101, 0xffff0000, v222
	v_mul_f32_e32 v104, 0.5, v104
	v_add_f32_e32 v103, 1.0, v103
	v_add_f32_e32 v101, v105, v101
	v_mul_f32_e32 v103, v104, v103
	v_mul_f32_e32 v101, v103, v101
	v_cvt_pk_bf16_f32 v103, v100, v101
	ds_read_b64 v[100:101], v116 offset:3200
	ds_write_b32 v190, v103 offset:3328
	s_waitcnt lgkmcnt(1)
	v_lshlrev_b32_e32 v104, 16, v100
	v_mul_f32_e32 v104, 0x3fb8aa3b, v104
	v_exp_f32_e32 v104, v104
	v_and_b32_e32 v103, 0xffff0000, v100
	v_lshlrev_b32_e32 v100, 16, v101
	v_mul_f32_e32 v100, 0x3fb8aa3b, v100
	v_fmac_f32_e32 v103, v102, v104
	v_lshlrev_b32_e32 v102, 16, v226
	v_mul_f32_e32 v104, 0x3d372713, v102
	v_mul_f32_e32 v104, v104, v102
	v_fma_f32 v104, v104, v102, v102
	v_mul_f32_e32 v104, 0x3f4c422a, v104
	v_add_f32_e32 v104, v104, v104
	v_mul_f32_e32 v104, 0x3fb8aa3b, v104
	v_exp_f32_e32 v104, v104
	v_exp_f32_e32 v100, v100
	v_and_b32_e32 v106, 0xffff0000, v101
	v_mul_f32_e32 v102, 0.5, v102
	v_add_f32_e32 v101, 1.0, v104
	v_and_b32_e32 v104, 0xffff0000, v226
	v_fmac_f32_e32 v106, v105, v100
	v_mul_f32_e32 v105, 0x3d372713, v104
	v_mul_f32_e32 v105, v105, v104
	v_fma_f32 v105, v105, v104, v104
	v_mul_f32_e32 v105, 0x3f4c422a, v105
	v_rcp_f32_e32 v101, v101
	v_add_f32_e32 v105, v105, v105
	v_mul_f32_e32 v105, 0x3fb8aa3b, v105
	v_exp_f32_e32 v105, v105
	v_fma_f32 v101, v101, -2.0, 1.0
	v_add_f32_e32 v101, 1.0, v101
	v_mul_f32_e32 v101, v102, v101
	v_add_f32_e32 v102, 1.0, v105
	v_rcp_f32_e32 v102, v102
	v_lshlrev_b32_e32 v100, 16, v220
	v_add_f32_e32 v100, v103, v100
	v_mul_f32_e32 v100, v101, v100
	v_fma_f32 v102, v102, -2.0, 1.0
	v_and_b32_e32 v101, 0xffff0000, v220
	v_mul_f32_e32 v104, 0.5, v104
	v_add_f32_e32 v102, 1.0, v102
	v_add_f32_e32 v101, v106, v101
	v_mul_f32_e32 v102, v104, v102
	v_mul_f32_e32 v101, v102, v101
	v_cvt_pk_bf16_f32 v102, v100, v101
	ds_read_b64 v[100:101], v116 offset:3072
	ds_write_b32 v190, v102 offset:3200
	s_waitcnt lgkmcnt(1)
	v_lshlrev_b32_e32 v104, 16, v100
	v_mul_f32_e32 v104, 0x3fb8aa3b, v104
	v_exp_f32_e32 v104, v104
	v_and_b32_e32 v102, 0xffff0000, v100
	v_lshlrev_b32_e32 v100, 16, v101
	v_mul_f32_e32 v100, 0x3fb8aa3b, v100
	v_fmac_f32_e32 v102, v103, v104
	v_lshlrev_b32_e32 v103, 16, v224
	v_mul_f32_e32 v104, 0x3d372713, v103
	v_mul_f32_e32 v104, v104, v103
	v_fma_f32 v104, v104, v103, v103
	v_mul_f32_e32 v104, 0x3f4c422a, v104
	v_add_f32_e32 v104, v104, v104
	v_mul_f32_e32 v104, 0x3fb8aa3b, v104
	v_exp_f32_e32 v104, v104
	v_exp_f32_e32 v100, v100
	v_and_b32_e32 v105, 0xffff0000, v101
	v_mul_f32_e32 v103, 0.5, v103
	v_add_f32_e32 v101, 1.0, v104
	v_and_b32_e32 v104, 0xffff0000, v224
	v_fmac_f32_e32 v105, v106, v100
	v_mul_f32_e32 v106, 0x3d372713, v104
	v_mul_f32_e32 v106, v106, v104
	v_fma_f32 v106, v106, v104, v104
	v_mul_f32_e32 v106, 0x3f4c422a, v106
	v_rcp_f32_e32 v101, v101
	v_add_f32_e32 v106, v106, v106
	v_mul_f32_e32 v106, 0x3fb8aa3b, v106
	v_exp_f32_e32 v106, v106
	v_fma_f32 v101, v101, -2.0, 1.0
	v_add_f32_e32 v101, 1.0, v101
	v_mul_f32_e32 v101, v103, v101
	v_add_f32_e32 v103, 1.0, v106
	v_rcp_f32_e32 v103, v103
	v_lshlrev_b32_e32 v100, 16, v218
	v_add_f32_e32 v100, v102, v100
	v_mul_f32_e32 v100, v101, v100
	v_fma_f32 v103, v103, -2.0, 1.0
	v_and_b32_e32 v101, 0xffff0000, v218
	v_mul_f32_e32 v104, 0.5, v104
	v_add_f32_e32 v103, 1.0, v103
	v_add_f32_e32 v101, v105, v101
	v_mul_f32_e32 v103, v104, v103
	v_mul_f32_e32 v101, v103, v101
	v_cvt_pk_bf16_f32 v103, v100, v101
	ds_read_b64 v[100:101], v116 offset:2944
	ds_write_b32 v190, v103 offset:3072
	s_waitcnt lgkmcnt(1)
	v_lshlrev_b32_e32 v104, 16, v100
	v_mul_f32_e32 v104, 0x3fb8aa3b, v104
	v_exp_f32_e32 v104, v104
	v_and_b32_e32 v103, 0xffff0000, v100
	v_lshlrev_b32_e32 v100, 16, v101
	v_mul_f32_e32 v100, 0x3fb8aa3b, v100
	v_fmac_f32_e32 v103, v102, v104
	v_lshlrev_b32_e32 v102, 16, v223
	v_mul_f32_e32 v104, 0x3d372713, v102
	v_mul_f32_e32 v104, v104, v102
	v_fma_f32 v104, v104, v102, v102
	v_mul_f32_e32 v104, 0x3f4c422a, v104
	v_add_f32_e32 v104, v104, v104
	v_mul_f32_e32 v104, 0x3fb8aa3b, v104
	v_exp_f32_e32 v104, v104
	v_exp_f32_e32 v100, v100
	v_and_b32_e32 v106, 0xffff0000, v101
	v_mul_f32_e32 v102, 0.5, v102
	v_add_f32_e32 v101, 1.0, v104
	v_and_b32_e32 v104, 0xffff0000, v223
	v_fmac_f32_e32 v106, v105, v100
	v_mul_f32_e32 v105, 0x3d372713, v104
	v_mul_f32_e32 v105, v105, v104
	v_fma_f32 v105, v105, v104, v104
	v_mul_f32_e32 v105, 0x3f4c422a, v105
	v_rcp_f32_e32 v101, v101
	v_add_f32_e32 v105, v105, v105
	v_mul_f32_e32 v105, 0x3fb8aa3b, v105
	v_exp_f32_e32 v105, v105
	v_fma_f32 v101, v101, -2.0, 1.0
	v_add_f32_e32 v101, 1.0, v101
	v_mul_f32_e32 v101, v102, v101
	v_add_f32_e32 v102, 1.0, v105
	v_rcp_f32_e32 v102, v102
	v_lshlrev_b32_e32 v100, 16, v216
	v_add_f32_e32 v100, v103, v100
	v_mul_f32_e32 v100, v101, v100
	v_fma_f32 v102, v102, -2.0, 1.0
	v_and_b32_e32 v101, 0xffff0000, v216
	v_mul_f32_e32 v104, 0.5, v104
	v_add_f32_e32 v102, 1.0, v102
	v_add_f32_e32 v101, v106, v101
	v_mul_f32_e32 v102, v104, v102
	v_mul_f32_e32 v101, v102, v101
	v_cvt_pk_bf16_f32 v102, v100, v101
	ds_read_b64 v[100:101], v116 offset:2816
	ds_write_b32 v190, v102 offset:2944
	s_waitcnt lgkmcnt(1)
	v_lshlrev_b32_e32 v104, 16, v100
	v_mul_f32_e32 v104, 0x3fb8aa3b, v104
	v_exp_f32_e32 v104, v104
	v_and_b32_e32 v102, 0xffff0000, v100
	v_lshlrev_b32_e32 v100, 16, v101
	v_mul_f32_e32 v100, 0x3fb8aa3b, v100
	v_fmac_f32_e32 v102, v103, v104
	v_lshlrev_b32_e32 v103, 16, v221
	v_mul_f32_e32 v104, 0x3d372713, v103
	v_mul_f32_e32 v104, v104, v103
	v_fma_f32 v104, v104, v103, v103
	v_mul_f32_e32 v104, 0x3f4c422a, v104
	v_add_f32_e32 v104, v104, v104
	v_mul_f32_e32 v104, 0x3fb8aa3b, v104
	v_exp_f32_e32 v104, v104
	v_exp_f32_e32 v100, v100
	v_and_b32_e32 v105, 0xffff0000, v101
	v_mul_f32_e32 v103, 0.5, v103
	v_add_f32_e32 v101, 1.0, v104
	v_and_b32_e32 v104, 0xffff0000, v221
	v_fmac_f32_e32 v105, v106, v100
	v_mul_f32_e32 v106, 0x3d372713, v104
	v_mul_f32_e32 v106, v106, v104
	v_fma_f32 v106, v106, v104, v104
	v_mul_f32_e32 v106, 0x3f4c422a, v106
	v_rcp_f32_e32 v101, v101
	v_add_f32_e32 v106, v106, v106
	v_mul_f32_e32 v106, 0x3fb8aa3b, v106
	v_exp_f32_e32 v106, v106
	v_fma_f32 v101, v101, -2.0, 1.0
	v_add_f32_e32 v101, 1.0, v101
	v_mul_f32_e32 v101, v103, v101
	v_add_f32_e32 v103, 1.0, v106
	v_rcp_f32_e32 v103, v103
	v_lshlrev_b32_e32 v100, 16, v214
	v_add_f32_e32 v100, v102, v100
	v_mul_f32_e32 v100, v101, v100
	v_fma_f32 v103, v103, -2.0, 1.0
	v_and_b32_e32 v101, 0xffff0000, v214
	v_mul_f32_e32 v104, 0.5, v104
	v_add_f32_e32 v103, 1.0, v103
	v_add_f32_e32 v101, v105, v101
	v_mul_f32_e32 v103, v104, v103
	v_mul_f32_e32 v101, v103, v101
	v_cvt_pk_bf16_f32 v103, v100, v101
	ds_read_b64 v[100:101], v116 offset:2688
	ds_write_b32 v190, v103 offset:2816
	s_waitcnt lgkmcnt(1)
	v_lshlrev_b32_e32 v104, 16, v100
	v_mul_f32_e32 v104, 0x3fb8aa3b, v104
	v_exp_f32_e32 v104, v104
	v_and_b32_e32 v103, 0xffff0000, v100
	v_lshlrev_b32_e32 v100, 16, v101
	v_mul_f32_e32 v100, 0x3fb8aa3b, v100
	v_fmac_f32_e32 v103, v102, v104
	v_lshlrev_b32_e32 v102, 16, v219
	v_mul_f32_e32 v104, 0x3d372713, v102
	v_mul_f32_e32 v104, v104, v102
	v_fma_f32 v104, v104, v102, v102
	v_mul_f32_e32 v104, 0x3f4c422a, v104
	v_add_f32_e32 v104, v104, v104
	v_mul_f32_e32 v104, 0x3fb8aa3b, v104
	v_exp_f32_e32 v104, v104
	v_exp_f32_e32 v100, v100
	v_and_b32_e32 v106, 0xffff0000, v101
	v_mul_f32_e32 v102, 0.5, v102
	v_add_f32_e32 v101, 1.0, v104
	v_and_b32_e32 v104, 0xffff0000, v219
	v_fmac_f32_e32 v106, v105, v100
	v_mul_f32_e32 v105, 0x3d372713, v104
	v_mul_f32_e32 v105, v105, v104
	v_fma_f32 v105, v105, v104, v104
	v_mul_f32_e32 v105, 0x3f4c422a, v105
	v_rcp_f32_e32 v101, v101
	v_add_f32_e32 v105, v105, v105
	v_mul_f32_e32 v105, 0x3fb8aa3b, v105
	v_exp_f32_e32 v105, v105
	v_fma_f32 v101, v101, -2.0, 1.0
	v_add_f32_e32 v101, 1.0, v101
	v_mul_f32_e32 v101, v102, v101
	v_add_f32_e32 v102, 1.0, v105
	v_rcp_f32_e32 v102, v102
	v_lshlrev_b32_e32 v100, 16, v211
	v_add_f32_e32 v100, v103, v100
	v_mul_f32_e32 v100, v101, v100
	v_fma_f32 v102, v102, -2.0, 1.0
	v_and_b32_e32 v101, 0xffff0000, v211
	v_mul_f32_e32 v104, 0.5, v104
	v_add_f32_e32 v102, 1.0, v102
	v_add_f32_e32 v101, v106, v101
	v_mul_f32_e32 v102, v104, v102
	v_mul_f32_e32 v101, v102, v101
	v_cvt_pk_bf16_f32 v102, v100, v101
	ds_read_b64 v[100:101], v116 offset:2560
	ds_write_b32 v190, v102 offset:2688
	s_waitcnt lgkmcnt(1)
	v_lshlrev_b32_e32 v104, 16, v100
	v_mul_f32_e32 v104, 0x3fb8aa3b, v104
	v_exp_f32_e32 v104, v104
	v_and_b32_e32 v102, 0xffff0000, v100
	v_lshlrev_b32_e32 v100, 16, v101
	v_mul_f32_e32 v100, 0x3fb8aa3b, v100
	v_fmac_f32_e32 v102, v103, v104
	v_lshlrev_b32_e32 v103, 16, v217
	v_mul_f32_e32 v104, 0x3d372713, v103
	v_mul_f32_e32 v104, v104, v103
	v_fma_f32 v104, v104, v103, v103
	v_mul_f32_e32 v104, 0x3f4c422a, v104
	v_add_f32_e32 v104, v104, v104
	v_mul_f32_e32 v104, 0x3fb8aa3b, v104
	v_exp_f32_e32 v104, v104
	v_exp_f32_e32 v100, v100
	v_and_b32_e32 v105, 0xffff0000, v101
	v_mul_f32_e32 v103, 0.5, v103
	v_add_f32_e32 v101, 1.0, v104
	v_and_b32_e32 v104, 0xffff0000, v217
	v_fmac_f32_e32 v105, v106, v100
	v_mul_f32_e32 v106, 0x3d372713, v104
	v_mul_f32_e32 v106, v106, v104
	v_fma_f32 v106, v106, v104, v104
	v_mul_f32_e32 v106, 0x3f4c422a, v106
	v_rcp_f32_e32 v101, v101
	v_add_f32_e32 v106, v106, v106
	v_mul_f32_e32 v106, 0x3fb8aa3b, v106
	v_exp_f32_e32 v106, v106
	v_fma_f32 v101, v101, -2.0, 1.0
	v_add_f32_e32 v101, 1.0, v101
	v_mul_f32_e32 v101, v103, v101
	v_add_f32_e32 v103, 1.0, v106
	v_rcp_f32_e32 v103, v103
	v_lshlrev_b32_e32 v100, 16, v209
	v_add_f32_e32 v100, v102, v100
	v_mul_f32_e32 v100, v101, v100
	v_fma_f32 v103, v103, -2.0, 1.0
	v_and_b32_e32 v101, 0xffff0000, v209
	v_mul_f32_e32 v104, 0.5, v104
	v_add_f32_e32 v103, 1.0, v103
	v_add_f32_e32 v101, v105, v101
	v_mul_f32_e32 v103, v104, v103
	v_mul_f32_e32 v101, v103, v101
	v_cvt_pk_bf16_f32 v103, v100, v101
	ds_read_b64 v[100:101], v116 offset:2432
	ds_write_b32 v190, v103 offset:2560
	s_waitcnt lgkmcnt(1)
	v_lshlrev_b32_e32 v104, 16, v100
	v_mul_f32_e32 v104, 0x3fb8aa3b, v104
	v_exp_f32_e32 v104, v104
	v_and_b32_e32 v103, 0xffff0000, v100
	v_lshlrev_b32_e32 v100, 16, v101
	v_mul_f32_e32 v100, 0x3fb8aa3b, v100
	v_fmac_f32_e32 v103, v102, v104
	v_lshlrev_b32_e32 v102, 16, v215
	v_mul_f32_e32 v104, 0x3d372713, v102
	v_mul_f32_e32 v104, v104, v102
	v_fma_f32 v104, v104, v102, v102
	v_mul_f32_e32 v104, 0x3f4c422a, v104
	v_add_f32_e32 v104, v104, v104
	v_mul_f32_e32 v104, 0x3fb8aa3b, v104
	v_exp_f32_e32 v104, v104
	v_exp_f32_e32 v100, v100
	v_and_b32_e32 v106, 0xffff0000, v101
	v_mul_f32_e32 v102, 0.5, v102
	v_add_f32_e32 v101, 1.0, v104
	v_and_b32_e32 v104, 0xffff0000, v215
	v_fmac_f32_e32 v106, v105, v100
	v_mul_f32_e32 v105, 0x3d372713, v104
	v_mul_f32_e32 v105, v105, v104
	v_fma_f32 v105, v105, v104, v104
	v_mul_f32_e32 v105, 0x3f4c422a, v105
	v_rcp_f32_e32 v101, v101
	v_add_f32_e32 v105, v105, v105
	v_mul_f32_e32 v105, 0x3fb8aa3b, v105
	v_exp_f32_e32 v105, v105
	v_fma_f32 v101, v101, -2.0, 1.0
	v_add_f32_e32 v101, 1.0, v101
	v_mul_f32_e32 v101, v102, v101
	v_add_f32_e32 v102, 1.0, v105
	v_rcp_f32_e32 v102, v102
	v_lshlrev_b32_e32 v100, 16, v207
	v_add_f32_e32 v100, v103, v100
	v_mul_f32_e32 v100, v101, v100
	v_fma_f32 v102, v102, -2.0, 1.0
	v_and_b32_e32 v101, 0xffff0000, v207
	v_mul_f32_e32 v104, 0.5, v104
	v_add_f32_e32 v102, 1.0, v102
	v_add_f32_e32 v101, v106, v101
	v_mul_f32_e32 v102, v104, v102
	v_mul_f32_e32 v101, v102, v101
	v_cvt_pk_bf16_f32 v102, v100, v101
	ds_read_b64 v[100:101], v116 offset:2304
	ds_write_b32 v190, v102 offset:2432
	s_waitcnt lgkmcnt(1)
	v_lshlrev_b32_e32 v104, 16, v100
	v_mul_f32_e32 v104, 0x3fb8aa3b, v104
	v_exp_f32_e32 v104, v104
	v_and_b32_e32 v102, 0xffff0000, v100
	v_lshlrev_b32_e32 v100, 16, v101
	v_mul_f32_e32 v100, 0x3fb8aa3b, v100
	v_fmac_f32_e32 v102, v103, v104
	v_lshlrev_b32_e32 v103, 16, v213
	v_mul_f32_e32 v104, 0x3d372713, v103
	v_mul_f32_e32 v104, v104, v103
	v_fma_f32 v104, v104, v103, v103
	v_mul_f32_e32 v104, 0x3f4c422a, v104
	v_add_f32_e32 v104, v104, v104
	v_mul_f32_e32 v104, 0x3fb8aa3b, v104
	v_exp_f32_e32 v104, v104
	v_exp_f32_e32 v100, v100
	v_and_b32_e32 v105, 0xffff0000, v101
	v_mul_f32_e32 v103, 0.5, v103
	v_add_f32_e32 v101, 1.0, v104
	v_and_b32_e32 v104, 0xffff0000, v213
	v_fmac_f32_e32 v105, v106, v100
	v_mul_f32_e32 v106, 0x3d372713, v104
	v_mul_f32_e32 v106, v106, v104
	v_fma_f32 v106, v106, v104, v104
	v_mul_f32_e32 v106, 0x3f4c422a, v106
	v_rcp_f32_e32 v101, v101
	v_add_f32_e32 v106, v106, v106
	v_mul_f32_e32 v106, 0x3fb8aa3b, v106
	v_exp_f32_e32 v106, v106
	v_fma_f32 v101, v101, -2.0, 1.0
	v_add_f32_e32 v101, 1.0, v101
	v_mul_f32_e32 v101, v103, v101
	v_add_f32_e32 v103, 1.0, v106
	v_rcp_f32_e32 v103, v103
	v_lshlrev_b32_e32 v100, 16, v205
	v_add_f32_e32 v100, v102, v100
	v_mul_f32_e32 v100, v101, v100
	v_fma_f32 v103, v103, -2.0, 1.0
	v_and_b32_e32 v101, 0xffff0000, v205
	v_mul_f32_e32 v104, 0.5, v104
	v_add_f32_e32 v103, 1.0, v103
	v_add_f32_e32 v101, v105, v101
	v_mul_f32_e32 v103, v104, v103
	v_mul_f32_e32 v101, v103, v101
	v_cvt_pk_bf16_f32 v103, v100, v101
	ds_read_b64 v[100:101], v116 offset:2176
	ds_write_b32 v190, v103 offset:2304
	s_waitcnt lgkmcnt(1)
	v_lshlrev_b32_e32 v104, 16, v100
	v_mul_f32_e32 v104, 0x3fb8aa3b, v104
	v_exp_f32_e32 v104, v104
	v_and_b32_e32 v103, 0xffff0000, v100
	v_lshlrev_b32_e32 v100, 16, v101
	v_mul_f32_e32 v100, 0x3fb8aa3b, v100
	v_fmac_f32_e32 v103, v102, v104
	v_lshlrev_b32_e32 v102, 16, v212
	v_mul_f32_e32 v104, 0x3d372713, v102
	v_mul_f32_e32 v104, v104, v102
	v_fma_f32 v104, v104, v102, v102
	v_mul_f32_e32 v104, 0x3f4c422a, v104
	v_add_f32_e32 v104, v104, v104
	v_mul_f32_e32 v104, 0x3fb8aa3b, v104
	v_exp_f32_e32 v104, v104
	v_exp_f32_e32 v100, v100
	v_and_b32_e32 v106, 0xffff0000, v101
	v_mul_f32_e32 v102, 0.5, v102
	v_add_f32_e32 v101, 1.0, v104
	v_and_b32_e32 v104, 0xffff0000, v212
	v_fmac_f32_e32 v106, v105, v100
	v_mul_f32_e32 v105, 0x3d372713, v104
	v_mul_f32_e32 v105, v105, v104
	v_fma_f32 v105, v105, v104, v104
	v_mul_f32_e32 v105, 0x3f4c422a, v105
	v_rcp_f32_e32 v101, v101
	v_add_f32_e32 v105, v105, v105
	v_mul_f32_e32 v105, 0x3fb8aa3b, v105
	v_exp_f32_e32 v105, v105
	v_fma_f32 v101, v101, -2.0, 1.0
	v_add_f32_e32 v101, 1.0, v101
	v_mul_f32_e32 v101, v102, v101
	v_add_f32_e32 v102, 1.0, v105
	v_rcp_f32_e32 v102, v102
	v_lshlrev_b32_e32 v100, 16, v203
	v_add_f32_e32 v100, v103, v100
	v_mul_f32_e32 v100, v101, v100
	v_fma_f32 v102, v102, -2.0, 1.0
	v_and_b32_e32 v101, 0xffff0000, v203
	v_mul_f32_e32 v104, 0.5, v104
	v_add_f32_e32 v102, 1.0, v102
	v_add_f32_e32 v101, v106, v101
	v_mul_f32_e32 v102, v104, v102
	v_mul_f32_e32 v101, v102, v101
	v_cvt_pk_bf16_f32 v102, v100, v101
	ds_read_b64 v[100:101], v116 offset:2048
	ds_write_b32 v190, v102 offset:2176
	s_waitcnt lgkmcnt(1)
	v_lshlrev_b32_e32 v104, 16, v100
	v_mul_f32_e32 v104, 0x3fb8aa3b, v104
	v_exp_f32_e32 v104, v104
	v_and_b32_e32 v102, 0xffff0000, v100
	v_lshlrev_b32_e32 v100, 16, v101
	v_mul_f32_e32 v100, 0x3fb8aa3b, v100
	v_fmac_f32_e32 v102, v103, v104
	v_lshlrev_b32_e32 v103, 16, v210
	v_mul_f32_e32 v104, 0x3d372713, v103
	v_mul_f32_e32 v104, v104, v103
	v_fma_f32 v104, v104, v103, v103
	v_mul_f32_e32 v104, 0x3f4c422a, v104
	v_add_f32_e32 v104, v104, v104
	v_mul_f32_e32 v104, 0x3fb8aa3b, v104
	v_exp_f32_e32 v104, v104
	v_exp_f32_e32 v100, v100
	v_and_b32_e32 v105, 0xffff0000, v101
	v_mul_f32_e32 v103, 0.5, v103
	v_add_f32_e32 v101, 1.0, v104
	v_and_b32_e32 v104, 0xffff0000, v210
	v_fmac_f32_e32 v105, v106, v100
	v_mul_f32_e32 v106, 0x3d372713, v104
	v_mul_f32_e32 v106, v106, v104
	v_fma_f32 v106, v106, v104, v104
	v_mul_f32_e32 v106, 0x3f4c422a, v106
	v_rcp_f32_e32 v101, v101
	v_add_f32_e32 v106, v106, v106
	v_mul_f32_e32 v106, 0x3fb8aa3b, v106
	v_exp_f32_e32 v106, v106
	v_fma_f32 v101, v101, -2.0, 1.0
	v_add_f32_e32 v101, 1.0, v101
	v_mul_f32_e32 v101, v103, v101
	v_add_f32_e32 v103, 1.0, v106
	v_rcp_f32_e32 v103, v103
	v_lshlrev_b32_e32 v100, 16, v201
	v_add_f32_e32 v100, v102, v100
	v_mul_f32_e32 v100, v101, v100
	v_fma_f32 v103, v103, -2.0, 1.0
	v_and_b32_e32 v101, 0xffff0000, v201
	v_mul_f32_e32 v104, 0.5, v104
	v_add_f32_e32 v103, 1.0, v103
	v_add_f32_e32 v101, v105, v101
	v_mul_f32_e32 v103, v104, v103
	v_mul_f32_e32 v101, v103, v101
	v_cvt_pk_bf16_f32 v103, v100, v101
	ds_read_b64 v[100:101], v116 offset:1920
	ds_write_b32 v190, v103 offset:2048
	s_waitcnt lgkmcnt(1)
	v_lshlrev_b32_e32 v104, 16, v100
	v_mul_f32_e32 v104, 0x3fb8aa3b, v104
	v_exp_f32_e32 v104, v104
	v_and_b32_e32 v103, 0xffff0000, v100
	v_lshlrev_b32_e32 v100, 16, v101
	v_mul_f32_e32 v100, 0x3fb8aa3b, v100
	v_fmac_f32_e32 v103, v102, v104
	v_lshlrev_b32_e32 v102, 16, v208
	v_mul_f32_e32 v104, 0x3d372713, v102
	v_mul_f32_e32 v104, v104, v102
	v_fma_f32 v104, v104, v102, v102
	v_mul_f32_e32 v104, 0x3f4c422a, v104
	v_add_f32_e32 v104, v104, v104
	v_mul_f32_e32 v104, 0x3fb8aa3b, v104
	v_exp_f32_e32 v104, v104
	v_exp_f32_e32 v100, v100
	v_and_b32_e32 v106, 0xffff0000, v101
	v_mul_f32_e32 v102, 0.5, v102
	v_add_f32_e32 v101, 1.0, v104
	v_and_b32_e32 v104, 0xffff0000, v208
	v_fmac_f32_e32 v106, v105, v100
	v_mul_f32_e32 v105, 0x3d372713, v104
	v_mul_f32_e32 v105, v105, v104
	v_fma_f32 v105, v105, v104, v104
	v_mul_f32_e32 v105, 0x3f4c422a, v105
	v_rcp_f32_e32 v101, v101
	v_add_f32_e32 v105, v105, v105
	v_mul_f32_e32 v105, 0x3fb8aa3b, v105
	v_exp_f32_e32 v105, v105
	v_fma_f32 v101, v101, -2.0, 1.0
	v_add_f32_e32 v101, 1.0, v101
	v_mul_f32_e32 v101, v102, v101
	v_add_f32_e32 v102, 1.0, v105
	v_rcp_f32_e32 v102, v102
	v_lshlrev_b32_e32 v100, 16, v198
	v_add_f32_e32 v100, v103, v100
	v_mul_f32_e32 v100, v101, v100
	v_fma_f32 v102, v102, -2.0, 1.0
	v_and_b32_e32 v101, 0xffff0000, v198
	v_mul_f32_e32 v104, 0.5, v104
	v_add_f32_e32 v102, 1.0, v102
	v_add_f32_e32 v101, v106, v101
	v_mul_f32_e32 v102, v104, v102
	v_mul_f32_e32 v101, v102, v101
	v_cvt_pk_bf16_f32 v102, v100, v101
	ds_read_b64 v[100:101], v116 offset:1792
	ds_write_b32 v190, v102 offset:1920
	s_waitcnt lgkmcnt(1)
	v_lshlrev_b32_e32 v104, 16, v100
	v_mul_f32_e32 v104, 0x3fb8aa3b, v104
	v_exp_f32_e32 v104, v104
	v_and_b32_e32 v102, 0xffff0000, v100
	v_lshlrev_b32_e32 v100, 16, v101
	v_mul_f32_e32 v100, 0x3fb8aa3b, v100
	v_fmac_f32_e32 v102, v103, v104
	v_lshlrev_b32_e32 v103, 16, v206
	v_mul_f32_e32 v104, 0x3d372713, v103
	v_mul_f32_e32 v104, v104, v103
	v_fma_f32 v104, v104, v103, v103
	v_mul_f32_e32 v104, 0x3f4c422a, v104
	v_add_f32_e32 v104, v104, v104
	v_mul_f32_e32 v104, 0x3fb8aa3b, v104
	v_exp_f32_e32 v104, v104
	v_exp_f32_e32 v100, v100
	v_and_b32_e32 v105, 0xffff0000, v101
	v_mul_f32_e32 v103, 0.5, v103
	v_add_f32_e32 v101, 1.0, v104
	v_and_b32_e32 v104, 0xffff0000, v206
	v_fmac_f32_e32 v105, v106, v100
	v_mul_f32_e32 v106, 0x3d372713, v104
	v_mul_f32_e32 v106, v106, v104
	v_fma_f32 v106, v106, v104, v104
	v_mul_f32_e32 v106, 0x3f4c422a, v106
	v_rcp_f32_e32 v101, v101
	v_add_f32_e32 v106, v106, v106
	v_mul_f32_e32 v106, 0x3fb8aa3b, v106
	v_exp_f32_e32 v106, v106
	v_fma_f32 v101, v101, -2.0, 1.0
	v_add_f32_e32 v101, 1.0, v101
	v_mul_f32_e32 v101, v103, v101
	v_add_f32_e32 v103, 1.0, v106
	v_rcp_f32_e32 v103, v103
	v_lshlrev_b32_e32 v100, 16, v196
	v_add_f32_e32 v100, v102, v100
	v_mul_f32_e32 v100, v101, v100
	v_fma_f32 v103, v103, -2.0, 1.0
	v_and_b32_e32 v101, 0xffff0000, v196
	v_mul_f32_e32 v104, 0.5, v104
	v_add_f32_e32 v103, 1.0, v103
	v_add_f32_e32 v101, v105, v101
	v_mul_f32_e32 v103, v104, v103
	v_mul_f32_e32 v101, v103, v101
	v_cvt_pk_bf16_f32 v103, v100, v101
	ds_read_b64 v[100:101], v116 offset:1664
	ds_write_b32 v190, v103 offset:1792
	s_waitcnt lgkmcnt(1)
	v_lshlrev_b32_e32 v104, 16, v100
	v_mul_f32_e32 v104, 0x3fb8aa3b, v104
	v_exp_f32_e32 v104, v104
	v_and_b32_e32 v103, 0xffff0000, v100
	v_lshlrev_b32_e32 v100, 16, v101
	v_mul_f32_e32 v100, 0x3fb8aa3b, v100
	v_fmac_f32_e32 v103, v102, v104
	v_lshlrev_b32_e32 v102, 16, v204
	v_mul_f32_e32 v104, 0x3d372713, v102
	v_mul_f32_e32 v104, v104, v102
	v_fma_f32 v104, v104, v102, v102
	v_mul_f32_e32 v104, 0x3f4c422a, v104
	v_add_f32_e32 v104, v104, v104
	v_mul_f32_e32 v104, 0x3fb8aa3b, v104
	v_exp_f32_e32 v104, v104
	v_exp_f32_e32 v100, v100
	v_and_b32_e32 v106, 0xffff0000, v101
	v_mul_f32_e32 v102, 0.5, v102
	v_add_f32_e32 v101, 1.0, v104
	v_and_b32_e32 v104, 0xffff0000, v204
	v_fmac_f32_e32 v106, v105, v100
	v_mul_f32_e32 v105, 0x3d372713, v104
	v_mul_f32_e32 v105, v105, v104
	v_fma_f32 v105, v105, v104, v104
	v_mul_f32_e32 v105, 0x3f4c422a, v105
	v_rcp_f32_e32 v101, v101
	v_add_f32_e32 v105, v105, v105
	v_mul_f32_e32 v105, 0x3fb8aa3b, v105
	v_exp_f32_e32 v105, v105
	v_fma_f32 v101, v101, -2.0, 1.0
	v_add_f32_e32 v101, 1.0, v101
	v_mul_f32_e32 v101, v102, v101
	v_add_f32_e32 v102, 1.0, v105
	v_rcp_f32_e32 v102, v102
	v_lshlrev_b32_e32 v100, 16, v194
	v_add_f32_e32 v100, v103, v100
	v_mul_f32_e32 v100, v101, v100
	v_fma_f32 v102, v102, -2.0, 1.0
	v_and_b32_e32 v101, 0xffff0000, v194
	v_mul_f32_e32 v104, 0.5, v104
	v_add_f32_e32 v102, 1.0, v102
	v_add_f32_e32 v101, v106, v101
	v_mul_f32_e32 v102, v104, v102
	v_mul_f32_e32 v101, v102, v101
	v_cvt_pk_bf16_f32 v102, v100, v101
	ds_read_b64 v[100:101], v116 offset:1536
	ds_write_b32 v190, v102 offset:1664
	s_waitcnt lgkmcnt(1)
	v_lshlrev_b32_e32 v104, 16, v100
	v_mul_f32_e32 v104, 0x3fb8aa3b, v104
	v_exp_f32_e32 v104, v104
	v_and_b32_e32 v102, 0xffff0000, v100
	v_lshlrev_b32_e32 v100, 16, v101
	v_mul_f32_e32 v100, 0x3fb8aa3b, v100
	v_fmac_f32_e32 v102, v103, v104
	v_lshlrev_b32_e32 v103, 16, v202
	v_mul_f32_e32 v104, 0x3d372713, v103
	v_mul_f32_e32 v104, v104, v103
	v_fma_f32 v104, v104, v103, v103
	v_mul_f32_e32 v104, 0x3f4c422a, v104
	v_add_f32_e32 v104, v104, v104
	v_mul_f32_e32 v104, 0x3fb8aa3b, v104
	v_exp_f32_e32 v104, v104
	v_exp_f32_e32 v100, v100
	v_and_b32_e32 v105, 0xffff0000, v101
	v_mul_f32_e32 v103, 0.5, v103
	v_add_f32_e32 v101, 1.0, v104
	v_and_b32_e32 v104, 0xffff0000, v202
	v_fmac_f32_e32 v105, v106, v100
	v_mul_f32_e32 v106, 0x3d372713, v104
	v_mul_f32_e32 v106, v106, v104
	v_fma_f32 v106, v106, v104, v104
	v_mul_f32_e32 v106, 0x3f4c422a, v106
	v_rcp_f32_e32 v101, v101
	v_add_f32_e32 v106, v106, v106
	v_mul_f32_e32 v106, 0x3fb8aa3b, v106
	v_exp_f32_e32 v106, v106
	v_fma_f32 v101, v101, -2.0, 1.0
	v_add_f32_e32 v101, 1.0, v101
	v_mul_f32_e32 v101, v103, v101
	v_add_f32_e32 v103, 1.0, v106
	v_rcp_f32_e32 v103, v103
	v_lshlrev_b32_e32 v100, 16, v157
	v_add_f32_e32 v100, v102, v100
	v_mul_f32_e32 v100, v101, v100
	v_fma_f32 v103, v103, -2.0, 1.0
	v_and_b32_e32 v101, 0xffff0000, v157
	v_mul_f32_e32 v104, 0.5, v104
	v_add_f32_e32 v103, 1.0, v103
	v_add_f32_e32 v101, v105, v101
	v_mul_f32_e32 v103, v104, v103
	v_mul_f32_e32 v101, v103, v101
	v_cvt_pk_bf16_f32 v103, v100, v101
	ds_read_b64 v[100:101], v116 offset:1408
	ds_write_b32 v190, v103 offset:1536
	s_waitcnt lgkmcnt(1)
	v_lshlrev_b32_e32 v104, 16, v100
	v_mul_f32_e32 v104, 0x3fb8aa3b, v104
	v_exp_f32_e32 v104, v104
	v_and_b32_e32 v103, 0xffff0000, v100
	v_lshlrev_b32_e32 v100, 16, v101
	v_mul_f32_e32 v100, 0x3fb8aa3b, v100
	v_fmac_f32_e32 v103, v102, v104
	v_lshlrev_b32_e32 v102, 16, v200
	v_mul_f32_e32 v104, 0x3d372713, v102
	v_mul_f32_e32 v104, v104, v102
	v_fma_f32 v104, v104, v102, v102
	v_mul_f32_e32 v104, 0x3f4c422a, v104
	v_add_f32_e32 v104, v104, v104
	v_mul_f32_e32 v104, 0x3fb8aa3b, v104
	v_exp_f32_e32 v104, v104
	v_exp_f32_e32 v100, v100
	v_and_b32_e32 v106, 0xffff0000, v101
	v_mul_f32_e32 v102, 0.5, v102
	v_add_f32_e32 v101, 1.0, v104
	v_and_b32_e32 v104, 0xffff0000, v200
	v_fmac_f32_e32 v106, v105, v100
	v_mul_f32_e32 v105, 0x3d372713, v104
	v_mul_f32_e32 v105, v105, v104
	v_fma_f32 v105, v105, v104, v104
	v_mul_f32_e32 v105, 0x3f4c422a, v105
	v_rcp_f32_e32 v101, v101
	v_add_f32_e32 v105, v105, v105
	v_mul_f32_e32 v105, 0x3fb8aa3b, v105
	v_exp_f32_e32 v105, v105
	v_fma_f32 v101, v101, -2.0, 1.0
	v_add_f32_e32 v101, 1.0, v101
	v_mul_f32_e32 v101, v102, v101
	v_add_f32_e32 v102, 1.0, v105
	v_rcp_f32_e32 v102, v102
	v_lshlrev_b32_e32 v100, 16, v155
	v_add_f32_e32 v100, v103, v100
	v_mul_f32_e32 v100, v101, v100
	v_fma_f32 v102, v102, -2.0, 1.0
	v_and_b32_e32 v101, 0xffff0000, v155
	v_mul_f32_e32 v104, 0.5, v104
	v_add_f32_e32 v102, 1.0, v102
	v_add_f32_e32 v101, v106, v101
	v_mul_f32_e32 v102, v104, v102
	v_mul_f32_e32 v101, v102, v101
	v_cvt_pk_bf16_f32 v102, v100, v101
	ds_read_b64 v[100:101], v116 offset:1280
	ds_write_b32 v190, v102 offset:1408
	s_waitcnt lgkmcnt(1)
	v_lshlrev_b32_e32 v104, 16, v100
	v_mul_f32_e32 v104, 0x3fb8aa3b, v104
	v_exp_f32_e32 v104, v104
	v_and_b32_e32 v102, 0xffff0000, v100
	v_lshlrev_b32_e32 v100, 16, v101
	v_mul_f32_e32 v100, 0x3fb8aa3b, v100
	v_fmac_f32_e32 v102, v103, v104
	v_lshlrev_b32_e32 v103, 16, v199
	v_mul_f32_e32 v104, 0x3d372713, v103
	v_mul_f32_e32 v104, v104, v103
	v_fma_f32 v104, v104, v103, v103
	v_mul_f32_e32 v104, 0x3f4c422a, v104
	v_add_f32_e32 v104, v104, v104
	v_mul_f32_e32 v104, 0x3fb8aa3b, v104
	v_exp_f32_e32 v104, v104
	v_exp_f32_e32 v100, v100
	v_and_b32_e32 v105, 0xffff0000, v101
	v_mul_f32_e32 v103, 0.5, v103
	v_add_f32_e32 v101, 1.0, v104
	v_and_b32_e32 v104, 0xffff0000, v199
	v_fmac_f32_e32 v105, v106, v100
	v_mul_f32_e32 v106, 0x3d372713, v104
	v_mul_f32_e32 v106, v106, v104
	v_fma_f32 v106, v106, v104, v104
	v_mul_f32_e32 v106, 0x3f4c422a, v106
	v_rcp_f32_e32 v101, v101
	v_add_f32_e32 v106, v106, v106
	v_mul_f32_e32 v106, 0x3fb8aa3b, v106
	v_exp_f32_e32 v106, v106
	v_fma_f32 v101, v101, -2.0, 1.0
	v_add_f32_e32 v101, 1.0, v101
	v_mul_f32_e32 v101, v103, v101
	v_add_f32_e32 v103, 1.0, v106
	v_rcp_f32_e32 v103, v103
	v_lshlrev_b32_e32 v100, 16, v152
	v_add_f32_e32 v100, v102, v100
	v_mul_f32_e32 v100, v101, v100
	v_fma_f32 v103, v103, -2.0, 1.0
	v_and_b32_e32 v101, 0xffff0000, v152
	v_mul_f32_e32 v104, 0.5, v104
	v_add_f32_e32 v103, 1.0, v103
	v_add_f32_e32 v101, v105, v101
	v_mul_f32_e32 v103, v104, v103
	v_mul_f32_e32 v101, v103, v101
	v_cvt_pk_bf16_f32 v103, v100, v101
	ds_read_b64 v[100:101], v116 offset:1152
	ds_write_b32 v190, v103 offset:1280
	s_waitcnt lgkmcnt(1)
	v_lshlrev_b32_e32 v104, 16, v100
	v_mul_f32_e32 v104, 0x3fb8aa3b, v104
	v_exp_f32_e32 v104, v104
	v_and_b32_e32 v103, 0xffff0000, v100
	v_lshlrev_b32_e32 v100, 16, v101
	v_mul_f32_e32 v100, 0x3fb8aa3b, v100
	v_fmac_f32_e32 v103, v102, v104
	v_lshlrev_b32_e32 v102, 16, v197
	v_mul_f32_e32 v104, 0x3d372713, v102
	v_mul_f32_e32 v104, v104, v102
	v_fma_f32 v104, v104, v102, v102
	v_mul_f32_e32 v104, 0x3f4c422a, v104
	v_add_f32_e32 v104, v104, v104
	v_mul_f32_e32 v104, 0x3fb8aa3b, v104
	v_exp_f32_e32 v104, v104
	v_exp_f32_e32 v100, v100
	v_and_b32_e32 v106, 0xffff0000, v101
	v_mul_f32_e32 v102, 0.5, v102
	v_add_f32_e32 v101, 1.0, v104
	v_and_b32_e32 v104, 0xffff0000, v197
	v_fmac_f32_e32 v106, v105, v100
	v_mul_f32_e32 v105, 0x3d372713, v104
	v_mul_f32_e32 v105, v105, v104
	v_fma_f32 v105, v105, v104, v104
	v_mul_f32_e32 v105, 0x3f4c422a, v105
	v_rcp_f32_e32 v101, v101
	v_add_f32_e32 v105, v105, v105
	v_mul_f32_e32 v105, 0x3fb8aa3b, v105
	v_exp_f32_e32 v105, v105
	v_fma_f32 v101, v101, -2.0, 1.0
	v_add_f32_e32 v101, 1.0, v101
	v_mul_f32_e32 v101, v102, v101
	v_add_f32_e32 v102, 1.0, v105
	v_rcp_f32_e32 v102, v102
	v_lshlrev_b32_e32 v100, 16, v150
	v_add_f32_e32 v100, v103, v100
	v_mul_f32_e32 v100, v101, v100
	v_fma_f32 v102, v102, -2.0, 1.0
	v_and_b32_e32 v101, 0xffff0000, v150
	v_mul_f32_e32 v104, 0.5, v104
	v_add_f32_e32 v102, 1.0, v102
	v_add_f32_e32 v101, v106, v101
	v_mul_f32_e32 v102, v104, v102
	v_mul_f32_e32 v101, v102, v101
	v_cvt_pk_bf16_f32 v102, v100, v101
	ds_read_b64 v[100:101], v116 offset:1024
	ds_write_b32 v190, v102 offset:1152
	s_waitcnt lgkmcnt(1)
	v_lshlrev_b32_e32 v104, 16, v100
	v_mul_f32_e32 v104, 0x3fb8aa3b, v104
	v_exp_f32_e32 v104, v104
	v_and_b32_e32 v102, 0xffff0000, v100
	v_lshlrev_b32_e32 v100, 16, v101
	v_mul_f32_e32 v100, 0x3fb8aa3b, v100
	v_fmac_f32_e32 v102, v103, v104
	v_lshlrev_b32_e32 v103, 16, v195
	v_mul_f32_e32 v104, 0x3d372713, v103
	v_mul_f32_e32 v104, v104, v103
	v_fma_f32 v104, v104, v103, v103
	v_mul_f32_e32 v104, 0x3f4c422a, v104
	v_add_f32_e32 v104, v104, v104
	v_mul_f32_e32 v104, 0x3fb8aa3b, v104
	v_exp_f32_e32 v104, v104
	v_exp_f32_e32 v100, v100
	v_and_b32_e32 v105, 0xffff0000, v101
	v_mul_f32_e32 v103, 0.5, v103
	v_add_f32_e32 v101, 1.0, v104
	v_and_b32_e32 v104, 0xffff0000, v195
	v_fmac_f32_e32 v105, v106, v100
	v_mul_f32_e32 v106, 0x3d372713, v104
	v_mul_f32_e32 v106, v106, v104
	v_fma_f32 v106, v106, v104, v104
	v_mul_f32_e32 v106, 0x3f4c422a, v106
	v_rcp_f32_e32 v101, v101
	v_add_f32_e32 v106, v106, v106
	v_mul_f32_e32 v106, 0x3fb8aa3b, v106
	v_exp_f32_e32 v106, v106
	v_fma_f32 v101, v101, -2.0, 1.0
	v_add_f32_e32 v101, 1.0, v101
	v_mul_f32_e32 v101, v103, v101
	v_add_f32_e32 v103, 1.0, v106
	v_rcp_f32_e32 v103, v103
	v_lshlrev_b32_e32 v100, 16, v148
	v_add_f32_e32 v100, v102, v100
	v_mul_f32_e32 v100, v101, v100
	v_fma_f32 v103, v103, -2.0, 1.0
	v_and_b32_e32 v101, 0xffff0000, v148
	v_mul_f32_e32 v104, 0.5, v104
	v_add_f32_e32 v103, 1.0, v103
	v_add_f32_e32 v101, v105, v101
	v_mul_f32_e32 v103, v104, v103
	v_mul_f32_e32 v101, v103, v101
	v_cvt_pk_bf16_f32 v103, v100, v101
	ds_read_b64 v[100:101], v116 offset:896
	ds_write_b32 v190, v103 offset:1024
	s_waitcnt lgkmcnt(1)
	v_lshlrev_b32_e32 v104, 16, v100
	v_mul_f32_e32 v104, 0x3fb8aa3b, v104
	v_exp_f32_e32 v104, v104
	v_and_b32_e32 v103, 0xffff0000, v100
	v_lshlrev_b32_e32 v100, 16, v101
	v_mul_f32_e32 v100, 0x3fb8aa3b, v100
	v_fmac_f32_e32 v103, v102, v104
	v_lshlrev_b32_e32 v102, 16, v193
	v_mul_f32_e32 v104, 0x3d372713, v102
	v_mul_f32_e32 v104, v104, v102
	v_fma_f32 v104, v104, v102, v102
	v_mul_f32_e32 v104, 0x3f4c422a, v104
	v_add_f32_e32 v104, v104, v104
	v_mul_f32_e32 v104, 0x3fb8aa3b, v104
	v_exp_f32_e32 v104, v104
	v_exp_f32_e32 v100, v100
	v_and_b32_e32 v106, 0xffff0000, v101
	v_mul_f32_e32 v102, 0.5, v102
	v_add_f32_e32 v101, 1.0, v104
	v_and_b32_e32 v104, 0xffff0000, v193
	v_fmac_f32_e32 v106, v105, v100
	v_mul_f32_e32 v105, 0x3d372713, v104
	v_mul_f32_e32 v105, v105, v104
	v_fma_f32 v105, v105, v104, v104
	v_mul_f32_e32 v105, 0x3f4c422a, v105
	v_rcp_f32_e32 v101, v101
	v_add_f32_e32 v105, v105, v105
	v_mul_f32_e32 v105, 0x3fb8aa3b, v105
	v_exp_f32_e32 v105, v105
	v_fma_f32 v101, v101, -2.0, 1.0
	v_add_f32_e32 v101, 1.0, v101
	v_mul_f32_e32 v101, v102, v101
	v_add_f32_e32 v102, 1.0, v105
	v_rcp_f32_e32 v102, v102
	v_lshlrev_b32_e32 v100, 16, v146
	v_add_f32_e32 v100, v103, v100
	v_mul_f32_e32 v100, v101, v100
	v_fma_f32 v102, v102, -2.0, 1.0
	v_and_b32_e32 v101, 0xffff0000, v146
	v_mul_f32_e32 v104, 0.5, v104
	v_add_f32_e32 v102, 1.0, v102
	v_add_f32_e32 v101, v106, v101
	v_mul_f32_e32 v102, v104, v102
	v_mul_f32_e32 v101, v102, v101
	v_cvt_pk_bf16_f32 v102, v100, v101
	ds_read_b64 v[100:101], v116 offset:768
	ds_write_b32 v190, v102 offset:896
	s_waitcnt lgkmcnt(1)
	v_lshlrev_b32_e32 v104, 16, v100
	v_mul_f32_e32 v104, 0x3fb8aa3b, v104
	v_exp_f32_e32 v104, v104
	v_and_b32_e32 v102, 0xffff0000, v100
	v_lshlrev_b32_e32 v100, 16, v101
	v_mul_f32_e32 v100, 0x3fb8aa3b, v100
	v_fmac_f32_e32 v102, v103, v104
	v_lshlrev_b32_e32 v103, 16, v156
	v_mul_f32_e32 v104, 0x3d372713, v103
	v_mul_f32_e32 v104, v104, v103
	v_fma_f32 v104, v104, v103, v103
	v_mul_f32_e32 v104, 0x3f4c422a, v104
	v_add_f32_e32 v104, v104, v104
	v_mul_f32_e32 v104, 0x3fb8aa3b, v104
	v_exp_f32_e32 v104, v104
	v_exp_f32_e32 v100, v100
	v_and_b32_e32 v105, 0xffff0000, v101
	v_mul_f32_e32 v103, 0.5, v103
	v_add_f32_e32 v101, 1.0, v104
	v_and_b32_e32 v104, 0xffff0000, v156
	v_fmac_f32_e32 v105, v106, v100
	v_mul_f32_e32 v106, 0x3d372713, v104
	v_mul_f32_e32 v106, v106, v104
	v_fma_f32 v106, v106, v104, v104
	v_mul_f32_e32 v106, 0x3f4c422a, v106
	v_rcp_f32_e32 v101, v101
	v_add_f32_e32 v106, v106, v106
	v_mul_f32_e32 v106, 0x3fb8aa3b, v106
	v_exp_f32_e32 v106, v106
	v_fma_f32 v101, v101, -2.0, 1.0
	v_add_f32_e32 v101, 1.0, v101
	v_mul_f32_e32 v101, v103, v101
	v_add_f32_e32 v103, 1.0, v106
	v_rcp_f32_e32 v103, v103
	v_lshlrev_b32_e32 v100, 16, v144
	v_add_f32_e32 v100, v102, v100
	v_mul_f32_e32 v100, v101, v100
	v_fma_f32 v103, v103, -2.0, 1.0
	v_and_b32_e32 v101, 0xffff0000, v144
	v_mul_f32_e32 v104, 0.5, v104
	v_add_f32_e32 v103, 1.0, v103
	v_add_f32_e32 v101, v105, v101
	v_mul_f32_e32 v103, v104, v103
	v_mul_f32_e32 v101, v103, v101
	v_cvt_pk_bf16_f32 v103, v100, v101
	ds_read_b64 v[100:101], v116 offset:640
	ds_write_b32 v190, v103 offset:768
	s_waitcnt lgkmcnt(1)
	v_lshlrev_b32_e32 v104, 16, v100
	v_mul_f32_e32 v104, 0x3fb8aa3b, v104
	v_exp_f32_e32 v104, v104
	v_and_b32_e32 v103, 0xffff0000, v100
	v_lshlrev_b32_e32 v100, 16, v101
	v_mul_f32_e32 v100, 0x3fb8aa3b, v100
	v_fmac_f32_e32 v103, v102, v104
	v_lshlrev_b32_e32 v102, 16, v154
	v_mul_f32_e32 v104, 0x3d372713, v102
	v_mul_f32_e32 v104, v104, v102
	v_fma_f32 v104, v104, v102, v102
	v_mul_f32_e32 v104, 0x3f4c422a, v104
	v_add_f32_e32 v104, v104, v104
	v_mul_f32_e32 v104, 0x3fb8aa3b, v104
	v_exp_f32_e32 v104, v104
	v_exp_f32_e32 v100, v100
	v_and_b32_e32 v106, 0xffff0000, v101
	v_mul_f32_e32 v102, 0.5, v102
	v_add_f32_e32 v101, 1.0, v104
	v_and_b32_e32 v104, 0xffff0000, v154
	v_fmac_f32_e32 v106, v105, v100
	v_mul_f32_e32 v105, 0x3d372713, v104
	v_mul_f32_e32 v105, v105, v104
	v_fma_f32 v105, v105, v104, v104
	v_mul_f32_e32 v105, 0x3f4c422a, v105
	v_rcp_f32_e32 v101, v101
	v_add_f32_e32 v105, v105, v105
	v_mul_f32_e32 v105, 0x3fb8aa3b, v105
	v_exp_f32_e32 v105, v105
	v_fma_f32 v101, v101, -2.0, 1.0
	v_add_f32_e32 v101, 1.0, v101
	v_mul_f32_e32 v101, v102, v101
	v_add_f32_e32 v102, 1.0, v105
	v_rcp_f32_e32 v102, v102
	v_lshlrev_b32_e32 v100, 16, v143
	v_add_f32_e32 v100, v103, v100
	v_mul_f32_e32 v100, v101, v100
	v_fma_f32 v102, v102, -2.0, 1.0
	v_and_b32_e32 v101, 0xffff0000, v143
	v_mul_f32_e32 v104, 0.5, v104
	v_add_f32_e32 v102, 1.0, v102
	v_add_f32_e32 v101, v106, v101
	v_mul_f32_e32 v102, v104, v102
	v_mul_f32_e32 v101, v102, v101
	v_cvt_pk_bf16_f32 v102, v100, v101
	ds_read_b64 v[100:101], v116 offset:512
	ds_write_b32 v190, v102 offset:640
	s_waitcnt lgkmcnt(1)
	v_lshlrev_b32_e32 v104, 16, v100
	v_mul_f32_e32 v104, 0x3fb8aa3b, v104
	v_exp_f32_e32 v104, v104
	v_and_b32_e32 v102, 0xffff0000, v100
	v_lshlrev_b32_e32 v100, 16, v101
	v_mul_f32_e32 v100, 0x3fb8aa3b, v100
	v_fmac_f32_e32 v102, v103, v104
	v_lshlrev_b32_e32 v103, 16, v153
	v_mul_f32_e32 v104, 0x3d372713, v103
	v_mul_f32_e32 v104, v104, v103
	v_fma_f32 v104, v104, v103, v103
	v_mul_f32_e32 v104, 0x3f4c422a, v104
	v_add_f32_e32 v104, v104, v104
	v_mul_f32_e32 v104, 0x3fb8aa3b, v104
	v_exp_f32_e32 v104, v104
	v_exp_f32_e32 v100, v100
	v_and_b32_e32 v105, 0xffff0000, v101
	v_mul_f32_e32 v103, 0.5, v103
	v_add_f32_e32 v101, 1.0, v104
	v_and_b32_e32 v104, 0xffff0000, v153
	v_fmac_f32_e32 v105, v106, v100
	v_mul_f32_e32 v106, 0x3d372713, v104
	v_mul_f32_e32 v106, v106, v104
	v_fma_f32 v106, v106, v104, v104
	v_mul_f32_e32 v106, 0x3f4c422a, v106
	v_rcp_f32_e32 v101, v101
	v_add_f32_e32 v106, v106, v106
	v_mul_f32_e32 v106, 0x3fb8aa3b, v106
	v_exp_f32_e32 v106, v106
	v_fma_f32 v101, v101, -2.0, 1.0
	v_add_f32_e32 v101, 1.0, v101
	v_mul_f32_e32 v101, v103, v101
	v_add_f32_e32 v103, 1.0, v106
	v_rcp_f32_e32 v103, v103
	v_lshlrev_b32_e32 v100, 16, v142
	v_add_f32_e32 v100, v102, v100
	v_mul_f32_e32 v100, v101, v100
	v_fma_f32 v103, v103, -2.0, 1.0
	v_and_b32_e32 v101, 0xffff0000, v142
	v_mul_f32_e32 v104, 0.5, v104
	v_add_f32_e32 v103, 1.0, v103
	v_add_f32_e32 v101, v105, v101
	v_mul_f32_e32 v103, v104, v103
	v_mul_f32_e32 v101, v103, v101
	v_cvt_pk_bf16_f32 v103, v100, v101
	ds_read_b64 v[100:101], v116 offset:384
	ds_write_b32 v190, v103 offset:512
	s_waitcnt lgkmcnt(1)
	v_lshlrev_b32_e32 v104, 16, v100
	v_mul_f32_e32 v104, 0x3fb8aa3b, v104
	v_exp_f32_e32 v104, v104
	v_and_b32_e32 v103, 0xffff0000, v100
	v_lshlrev_b32_e32 v100, 16, v101
	v_mul_f32_e32 v100, 0x3fb8aa3b, v100
	v_fmac_f32_e32 v103, v102, v104
	v_lshlrev_b32_e32 v102, 16, v151
	v_mul_f32_e32 v104, 0x3d372713, v102
	v_mul_f32_e32 v104, v104, v102
	v_fma_f32 v104, v104, v102, v102
	v_mul_f32_e32 v104, 0x3f4c422a, v104
	v_add_f32_e32 v104, v104, v104
	v_mul_f32_e32 v104, 0x3fb8aa3b, v104
	v_exp_f32_e32 v104, v104
	v_exp_f32_e32 v100, v100
	v_and_b32_e32 v106, 0xffff0000, v101
	v_mul_f32_e32 v102, 0.5, v102
	v_add_f32_e32 v101, 1.0, v104
	v_and_b32_e32 v104, 0xffff0000, v151
	v_fmac_f32_e32 v106, v105, v100
	v_mul_f32_e32 v105, 0x3d372713, v104
	v_mul_f32_e32 v105, v105, v104
	v_fma_f32 v105, v105, v104, v104
	v_mul_f32_e32 v105, 0x3f4c422a, v105
	v_rcp_f32_e32 v101, v101
	v_add_f32_e32 v105, v105, v105
	v_mul_f32_e32 v105, 0x3fb8aa3b, v105
	v_exp_f32_e32 v105, v105
	v_fma_f32 v101, v101, -2.0, 1.0
	v_add_f32_e32 v101, 1.0, v101
	v_mul_f32_e32 v101, v102, v101
	v_add_f32_e32 v102, 1.0, v105
	v_rcp_f32_e32 v102, v102
	v_lshlrev_b32_e32 v100, 16, v141
	v_add_f32_e32 v100, v103, v100
	v_mul_f32_e32 v100, v101, v100
	v_fma_f32 v102, v102, -2.0, 1.0
	v_and_b32_e32 v101, 0xffff0000, v141
	v_mul_f32_e32 v104, 0.5, v104
	v_add_f32_e32 v102, 1.0, v102
	v_add_f32_e32 v101, v106, v101
	v_mul_f32_e32 v102, v104, v102
	v_mul_f32_e32 v101, v102, v101
	v_cvt_pk_bf16_f32 v102, v100, v101
	ds_read_b64 v[100:101], v116 offset:256
	ds_write_b32 v190, v102 offset:384
	s_waitcnt lgkmcnt(1)
	v_lshlrev_b32_e32 v104, 16, v100
	v_mul_f32_e32 v104, 0x3fb8aa3b, v104
	v_exp_f32_e32 v104, v104
	v_and_b32_e32 v102, 0xffff0000, v100
	v_lshlrev_b32_e32 v100, 16, v101
	v_mul_f32_e32 v100, 0x3fb8aa3b, v100
	v_fmac_f32_e32 v102, v103, v104
	v_lshlrev_b32_e32 v103, 16, v149
	v_mul_f32_e32 v104, 0x3d372713, v103
	v_mul_f32_e32 v104, v104, v103
	v_fma_f32 v104, v104, v103, v103
	v_mul_f32_e32 v104, 0x3f4c422a, v104
	v_add_f32_e32 v104, v104, v104
	v_mul_f32_e32 v104, 0x3fb8aa3b, v104
	v_exp_f32_e32 v104, v104
	v_exp_f32_e32 v100, v100
	v_and_b32_e32 v105, 0xffff0000, v101
	v_mul_f32_e32 v103, 0.5, v103
	v_add_f32_e32 v101, 1.0, v104
	v_and_b32_e32 v104, 0xffff0000, v149
	v_fmac_f32_e32 v105, v106, v100
	v_mul_f32_e32 v106, 0x3d372713, v104
	v_mul_f32_e32 v106, v106, v104
	v_fma_f32 v106, v106, v104, v104
	v_mul_f32_e32 v106, 0x3f4c422a, v106
	v_rcp_f32_e32 v101, v101
	v_add_f32_e32 v106, v106, v106
	v_mul_f32_e32 v106, 0x3fb8aa3b, v106
	v_exp_f32_e32 v106, v106
	v_fma_f32 v101, v101, -2.0, 1.0
	v_add_f32_e32 v101, 1.0, v101
	v_mul_f32_e32 v101, v103, v101
	v_add_f32_e32 v103, 1.0, v106
	v_rcp_f32_e32 v103, v103
	v_lshlrev_b32_e32 v100, 16, v140
	v_add_f32_e32 v100, v102, v100
	v_mul_f32_e32 v100, v101, v100
	v_fma_f32 v103, v103, -2.0, 1.0
	v_and_b32_e32 v101, 0xffff0000, v140
	v_mul_f32_e32 v104, 0.5, v104
	v_add_f32_e32 v103, 1.0, v103
	v_add_f32_e32 v101, v105, v101
	v_mul_f32_e32 v103, v104, v103
	v_mul_f32_e32 v101, v103, v101
	v_cvt_pk_bf16_f32 v103, v100, v101
	ds_read_b64 v[100:101], v116 offset:128
	ds_write_b32 v190, v103 offset:256
	s_waitcnt lgkmcnt(1)
	v_lshlrev_b32_e32 v104, 16, v100
	v_mul_f32_e32 v104, 0x3fb8aa3b, v104
	v_exp_f32_e32 v104, v104
	v_and_b32_e32 v103, 0xffff0000, v100
	v_lshlrev_b32_e32 v100, 16, v101
	v_mul_f32_e32 v100, 0x3fb8aa3b, v100
	v_fmac_f32_e32 v103, v102, v104
	v_lshlrev_b32_e32 v102, 16, v147
	v_mul_f32_e32 v104, 0x3d372713, v102
	v_mul_f32_e32 v104, v104, v102
	v_fma_f32 v104, v104, v102, v102
	v_mul_f32_e32 v104, 0x3f4c422a, v104
	v_add_f32_e32 v104, v104, v104
	v_mul_f32_e32 v104, 0x3fb8aa3b, v104
	v_exp_f32_e32 v104, v104
	v_exp_f32_e32 v100, v100
	v_and_b32_e32 v106, 0xffff0000, v101
	v_mul_f32_e32 v102, 0.5, v102
	v_add_f32_e32 v101, 1.0, v104
	v_and_b32_e32 v104, 0xffff0000, v147
	v_fmac_f32_e32 v106, v105, v100
	v_mul_f32_e32 v105, 0x3d372713, v104
	v_mul_f32_e32 v105, v105, v104
	v_fma_f32 v105, v105, v104, v104
	v_mul_f32_e32 v105, 0x3f4c422a, v105
	v_rcp_f32_e32 v101, v101
	v_add_f32_e32 v105, v105, v105
	v_mul_f32_e32 v105, 0x3fb8aa3b, v105
	v_exp_f32_e32 v105, v105
	v_fma_f32 v101, v101, -2.0, 1.0
	v_add_f32_e32 v101, 1.0, v101
	v_mul_f32_e32 v101, v102, v101
	v_add_f32_e32 v102, 1.0, v105
	v_rcp_f32_e32 v102, v102
	v_lshlrev_b32_e32 v100, 16, v139
	v_add_f32_e32 v100, v103, v100
	v_mul_f32_e32 v100, v101, v100
	v_fma_f32 v102, v102, -2.0, 1.0
	v_and_b32_e32 v101, 0xffff0000, v139
	v_mul_f32_e32 v104, 0.5, v104
	v_add_f32_e32 v102, 1.0, v102
	v_add_f32_e32 v101, v106, v101
	v_mul_f32_e32 v102, v104, v102
	v_mul_f32_e32 v101, v102, v101
	v_cvt_pk_bf16_f32 v102, v100, v101
	ds_read_b64 v[100:101], v116
	ds_write_b32 v190, v102 offset:128
	s_waitcnt lgkmcnt(1)
	v_lshlrev_b32_e32 v104, 16, v100
	v_mul_f32_e32 v104, 0x3fb8aa3b, v104
	v_exp_f32_e32 v104, v104
	v_and_b32_e32 v100, 0xffff0000, v100
	v_lshlrev_b32_e32 v102, 16, v101
	v_mul_f32_e32 v102, 0x3fb8aa3b, v102
	v_fmac_f32_e32 v100, v103, v104
	v_lshlrev_b32_e32 v103, 16, v145
	v_mul_f32_e32 v104, 0x3d372713, v103
	v_mul_f32_e32 v104, v104, v103
	v_fma_f32 v104, v104, v103, v103
	v_mul_f32_e32 v104, 0x3f4c422a, v104
	v_add_f32_e32 v104, v104, v104
	v_mul_f32_e32 v104, 0x3fb8aa3b, v104
	v_exp_f32_e32 v104, v104
	v_exp_f32_e32 v102, v102
	v_and_b32_e32 v101, 0xffff0000, v101
	v_mul_f32_e32 v103, 0.5, v103
	v_add_f32_e32 v104, 1.0, v104
	v_rcp_f32_e32 v104, v104
	v_fmac_f32_e32 v101, v106, v102
	v_lshlrev_b32_e32 v102, 16, v138
	v_add_f32_e32 v100, v100, v102
	v_fma_f32 v102, v104, -2.0, 1.0
	v_and_b32_e32 v104, 0xffff0000, v145
	v_mul_f32_e32 v105, 0x3d372713, v104
	v_mul_f32_e32 v105, v105, v104
	v_fma_f32 v105, v105, v104, v104
	v_mul_f32_e32 v105, 0x3f4c422a, v105
	v_add_f32_e32 v105, v105, v105
	v_mul_f32_e32 v105, 0x3fb8aa3b, v105
	v_exp_f32_e32 v105, v105
	v_add_f32_e32 v102, 1.0, v102
	v_mul_f32_e32 v102, v103, v102
	v_mul_f32_e32 v100, v102, v100
	v_add_f32_e32 v103, 1.0, v105
	v_rcp_f32_e32 v103, v103
	v_and_b32_e32 v102, 0xffff0000, v138
	v_add_f32_e32 v101, v101, v102
	v_fma_f32 v102, v103, -2.0, 1.0
	v_mul_f32_e32 v103, 0.5, v104
	v_add_f32_e32 v102, 1.0, v102
	v_mul_f32_e32 v102, v103, v102
	v_mul_f32_e32 v101, v102, v101
	v_cvt_pk_bf16_f32 v100, v100, v101
	ds_write_b32 v190, v100
	v_or_b32_e32 v102, s44, v72
	v_mov_b64_e32 v[100:101], s[20:21]
	v_mad_u64_u32 v[100:101], s[48:49], v102, s52, v[100:101]
	v_mad_i32_i24 v101, s45, v192, v101
	v_lshl_add_u64 v[100:101], s[42:43], 1, v[100:101]
	v_lshl_add_u64 v[100:101], v[100:101], 0, s[36:37]
	v_lshl_add_u64 v[104:105], v[100:101], 0, v[70:71]
	ds_read_b128 v[100:103], v191
	s_waitcnt lgkmcnt(0)
	global_store_dwordx4 v[104:105], v[100:103], off
	v_lshl_add_u64 v[104:105], v[104:105], 0, s[40:41]
	ds_read_b128 v[100:103], v191 offset:2048
	s_waitcnt lgkmcnt(0)
	global_store_dwordx4 v[104:105], v[100:103], off
	v_lshl_add_u64 v[104:105], v[104:105], 0, s[40:41]
	ds_read_b128 v[100:103], v191 offset:4224
	s_waitcnt lgkmcnt(0)
	global_store_dwordx4 v[104:105], v[100:103], off
	v_lshl_add_u64 v[104:105], v[104:105], 0, s[40:41]
	ds_read_b128 v[100:103], v191 offset:6272
	s_waitcnt lgkmcnt(0)
	global_store_dwordx4 v[104:105], v[100:103], off
	v_lshl_add_u64 v[104:105], v[104:105], 0, s[40:41]
	ds_read_b128 v[100:103], v191 offset:8448
	s_waitcnt lgkmcnt(0)
	global_store_dwordx4 v[104:105], v[100:103], off
	v_lshl_add_u64 v[104:105], v[104:105], 0, s[40:41]
	ds_read_b128 v[100:103], v191 offset:10496
	s_waitcnt lgkmcnt(0)
	global_store_dwordx4 v[104:105], v[100:103], off
	v_lshl_add_u64 v[104:105], v[104:105], 0, s[40:41]
	ds_read_b128 v[100:103], v191 offset:12672
	s_waitcnt lgkmcnt(0)
	global_store_dwordx4 v[104:105], v[100:103], off
	v_lshl_add_u64 v[104:105], v[104:105], 0, s[40:41]
	ds_read_b128 v[100:103], v191 offset:14720
	s_waitcnt lgkmcnt(0)
	global_store_dwordx4 v[104:105], v[100:103], off
	s_cbranch_vccz .LBB0_1505

.LBB0_1503:
	s_or_b64 exec, exec, s[48:49]
	s_ashr_i32 s45, s44, 31
	v_readlane_b32 s43, v254, 9
	s_ashr_i32 s47, s46, 31
	s_add_i32 s53, s53, s43
	s_lshl_b64 s[44:45], s[44:45], 7
	s_lshl_b64 s[46:47], s[46:47], 17
	s_add_u32 s46, s31, s46
	s_addc_u32 s47, s33, s47
	ds_write_b128 v173, v[22:25]
	s_waitcnt lgkmcnt(0)
	ds_write_b128 v174, v[2:5]
	ds_write_b128 v175, v[6:9]
	ds_write_b128 v176, v[10:13]
	ds_write_b128 v177, v[14:17] offset:128
	ds_write_b128 v178, v[18:21] offset:128
	ds_write_b128 v179, v[26:29] offset:128
	ds_write_b128 v180, v[30:33] offset:128
	ds_write_b128 v181, v[34:37] offset:256
	ds_write_b128 v182, v[38:41] offset:256
	ds_write_b128 v183, v[42:45] offset:256
	ds_write_b128 v184, v[46:49] offset:256
	ds_write_b128 v185, v[50:53] offset:384
	ds_write_b128 v186, v[54:57] offset:384
	ds_write_b128 v187, v[58:61] offset:384
	ds_write_b128 v188, v[62:65] offset:384
	v_lshl_add_u64 v[10:11], s[46:47], 0, v[66:67]
	v_lshl_add_u64 v[14:15], s[46:47], 0, v[74:75]
	v_lshl_add_u64 v[18:19], s[46:47], 0, v[76:77]
	v_lshl_add_u64 v[26:27], s[46:47], 0, v[78:79]
	v_lshl_add_u64 v[30:31], s[46:47], 0, v[80:81]
	v_lshl_add_u64 v[34:35], s[46:47], 0, v[82:83]
	v_lshl_add_u64 v[38:39], s[46:47], 0, v[84:85]
	v_lshl_add_u64 v[42:43], s[46:47], 0, v[86:87]
	v_lshl_add_u64 v[46:47], s[46:47], 0, v[88:89]
	global_load_dwordx4 v[22:25], v[10:11], off nt
	global_load_dwordx4 v[2:5], v[10:11], off offset:1024 nt
	global_load_dwordx4 v[6:9], v[10:11], off offset:2048 nt
	s_nop 0
	global_load_dwordx4 v[10:13], v[10:11], off offset:3072 nt
	s_nop 0
	global_load_dwordx4 v[14:17], v[14:15], off nt
	s_nop 0
	global_load_dwordx4 v[18:21], v[18:19], off nt
	s_nop 0
	global_load_dwordx4 v[26:29], v[26:27], off nt
	s_nop 0
	global_load_dwordx4 v[30:33], v[30:31], off nt
	s_nop 0
	global_load_dwordx4 v[34:37], v[34:35], off nt
	s_nop 0
	global_load_dwordx4 v[38:41], v[38:39], off nt
	s_nop 0
	global_load_dwordx4 v[42:45], v[42:43], off nt
	s_nop 0
	global_load_dwordx4 v[46:49], v[46:47], off nt
	ds_read2_b64 v[60:63], v189 offset1:16
	s_waitcnt lgkmcnt(14)
	v_pk_fma_f32 v[148:149], v[148:149], 0, v[152:153] op_sel_hi:[1,0,1]
	v_lshl_add_u64 v[50:51], s[46:47], 0, v[90:91]
	v_pk_fma_f32 v[144:145], v[148:149], v[144:145], v[150:151]
	v_lshl_add_u64 v[54:55], s[46:47], 0, v[92:93]
	s_waitcnt lgkmcnt(0)
	v_lshlrev_b32_e32 v64, 16, v60
	v_pk_fma_f32 v[140:141], v[144:145], v[140:141], v[146:147]
	v_lshlrev_b32_e32 v65, 16, v61
	v_add_f32_e32 v144, 0, v64
	v_mul_f32_e32 v64, 0x3fb8aa3b, v64
	v_pk_fma_f32 v[138:139], v[140:141], v[138:139], v[142:143]
	v_exp_f32_e32 v142, v64
	v_mul_f32_e32 v64, 0x3fb8aa3b, v65
	v_add_f32_e32 v145, 0, v65
	v_exp_f32_e32 v143, v64
	v_lshlrev_b32_e32 v64, 16, v62
	v_lshlrev_b32_e32 v65, 16, v63
	global_load_dwordx4 v[50:53], v[50:51], off nt
	s_nop 0
	global_load_dwordx4 v[54:57], v[54:55], off nt
	v_add_f32_e32 v148, v144, v64
	v_add_f32_e32 v149, v145, v65
	v_mul_f32_e32 v64, 0x3fb8aa3b, v64
	ds_read2_b64 v[144:147], v189 offset0:32 offset1:48
	v_exp_f32_e32 v64, v64
	v_mul_f32_e32 v65, 0x3fb8aa3b, v65
	v_exp_f32_e32 v65, v65
	v_and_b32_e32 v141, 0xffff0000, v60
	v_fma_f32 v60, 0, v142, v141
	v_and_b32_e32 v140, 0xffff0000, v61
	v_and_b32_e32 v62, 0xffff0000, v62
	v_fma_f32 v61, 0, v143, v140
	v_fmac_f32_e32 v62, v64, v60
	v_and_b32_e32 v60, 0xffff0000, v63
	s_waitcnt lgkmcnt(0)
	v_lshlrev_b32_e32 v63, 16, v145
	v_fmac_f32_e32 v60, v65, v61
	v_lshlrev_b32_e32 v61, 16, v144
	v_add_f32_e32 v65, v149, v63
	v_mul_f32_e32 v63, 0x3fb8aa3b, v63
	v_add_f32_e32 v64, v148, v61
	v_mul_f32_e32 v61, 0x3fb8aa3b, v61
	v_exp_f32_e32 v63, v63
	v_exp_f32_e32 v61, v61
	v_and_b32_e32 v145, 0xffff0000, v145
	v_and_b32_e32 v144, 0xffff0000, v144
	v_fmac_f32_e32 v145, v63, v60
	v_lshlrev_b32_e32 v60, 16, v146
	v_fmac_f32_e32 v144, v61, v62
	v_lshlrev_b32_e32 v61, 16, v147
	v_add_f32_e32 v64, v64, v60
	v_mul_f32_e32 v60, 0x3fb8aa3b, v60
	v_exp_f32_e32 v148, v60
	v_mul_f32_e32 v60, 0x3fb8aa3b, v61
	v_add_f32_e32 v65, v65, v61
	v_exp_f32_e32 v149, v60
	ds_read2_b64 v[60:63], v189 offset0:64 offset1:80
	v_and_b32_e32 v146, 0xffff0000, v146
	v_fmac_f32_e32 v146, v148, v144
	v_and_b32_e32 v144, 0xffff0000, v147
	v_fmac_f32_e32 v144, v149, v145
	s_waitcnt lgkmcnt(0)
	v_lshlrev_b32_e32 v147, 16, v61
	v_lshlrev_b32_e32 v145, 16, v60
	v_add_f32_e32 v65, v65, v147
	v_mul_f32_e32 v147, 0x3fb8aa3b, v147
	v_add_f32_e32 v64, v64, v145
	v_mul_f32_e32 v145, 0x3fb8aa3b, v145
	v_exp_f32_e32 v147, v147
	v_exp_f32_e32 v145, v145
	v_and_b32_e32 v61, 0xffff0000, v61
	v_and_b32_e32 v60, 0xffff0000, v60
	v_fmac_f32_e32 v61, v147, v144
	v_lshlrev_b32_e32 v144, 16, v62
	v_fmac_f32_e32 v60, v145, v146
	v_lshlrev_b32_e32 v145, 16, v63
	v_add_f32_e32 v64, v64, v144
	v_mul_f32_e32 v144, 0x3fb8aa3b, v144
	v_exp_f32_e32 v148, v144
	v_mul_f32_e32 v144, 0x3fb8aa3b, v145
	v_add_f32_e32 v65, v65, v145
	v_exp_f32_e32 v149, v144
	ds_read2_b64 v[144:147], v189 offset0:96 offset1:112
	v_and_b32_e32 v62, 0xffff0000, v62
	v_fmac_f32_e32 v62, v148, v60
	v_and_b32_e32 v60, 0xffff0000, v63
	v_fmac_f32_e32 v60, v149, v61
	s_waitcnt lgkmcnt(0)
	v_lshlrev_b32_e32 v63, 16, v145
	v_lshlrev_b32_e32 v61, 16, v144
	v_add_f32_e32 v65, v65, v63
	v_mul_f32_e32 v63, 0x3fb8aa3b, v63
	v_add_f32_e32 v64, v64, v61
	v_mul_f32_e32 v61, 0x3fb8aa3b, v61
	v_exp_f32_e32 v63, v63
	v_exp_f32_e32 v61, v61
	v_and_b32_e32 v145, 0xffff0000, v145
	v_and_b32_e32 v144, 0xffff0000, v144
	v_fmac_f32_e32 v145, v63, v60
	v_lshlrev_b32_e32 v60, 16, v146
	v_fmac_f32_e32 v144, v61, v62
	v_lshlrev_b32_e32 v61, 16, v147
	v_add_f32_e32 v64, v64, v60
	v_mul_f32_e32 v60, 0x3fb8aa3b, v60
	v_exp_f32_e32 v148, v60
	v_mul_f32_e32 v60, 0x3fb8aa3b, v61
	v_add_f32_e32 v65, v65, v61
	v_exp_f32_e32 v149, v60
	ds_read2_b64 v[60:63], v189 offset0:128 offset1:144
	v_and_b32_e32 v146, 0xffff0000, v146
	v_fmac_f32_e32 v146, v148, v144
	v_and_b32_e32 v144, 0xffff0000, v147
	v_fmac_f32_e32 v144, v149, v145
	s_waitcnt lgkmcnt(0)
	v_lshlrev_b32_e32 v147, 16, v61
	v_lshlrev_b32_e32 v145, 16, v60
	v_add_f32_e32 v65, v65, v147
	v_mul_f32_e32 v147, 0x3fb8aa3b, v147
	v_add_f32_e32 v64, v64, v145
	v_mul_f32_e32 v145, 0x3fb8aa3b, v145
	v_exp_f32_e32 v147, v147
	v_exp_f32_e32 v145, v145
	v_and_b32_e32 v61, 0xffff0000, v61
	v_and_b32_e32 v60, 0xffff0000, v60
	v_fmac_f32_e32 v61, v147, v144
	v_lshlrev_b32_e32 v144, 16, v62
	v_fmac_f32_e32 v60, v145, v146
	v_lshlrev_b32_e32 v145, 16, v63
	v_add_f32_e32 v64, v64, v144
	v_mul_f32_e32 v144, 0x3fb8aa3b, v144
	v_exp_f32_e32 v148, v144
	v_mul_f32_e32 v144, 0x3fb8aa3b, v145
	v_add_f32_e32 v65, v65, v145
	v_exp_f32_e32 v149, v144
	ds_read2_b64 v[144:147], v189 offset0:160 offset1:176
	v_and_b32_e32 v62, 0xffff0000, v62
	v_fmac_f32_e32 v62, v148, v60
	v_and_b32_e32 v60, 0xffff0000, v63
	v_fmac_f32_e32 v60, v149, v61
	s_waitcnt lgkmcnt(0)
	v_lshlrev_b32_e32 v63, 16, v145
	v_lshlrev_b32_e32 v61, 16, v144
	v_add_f32_e32 v65, v65, v63
	v_mul_f32_e32 v63, 0x3fb8aa3b, v63
	v_add_f32_e32 v64, v64, v61
	v_mul_f32_e32 v61, 0x3fb8aa3b, v61
	v_exp_f32_e32 v63, v63
	v_exp_f32_e32 v61, v61
	v_and_b32_e32 v145, 0xffff0000, v145
	v_and_b32_e32 v144, 0xffff0000, v144
	v_fmac_f32_e32 v145, v63, v60
	v_lshlrev_b32_e32 v60, 16, v146
	v_fmac_f32_e32 v144, v61, v62
	v_lshlrev_b32_e32 v61, 16, v147
	v_add_f32_e32 v64, v64, v60
	v_mul_f32_e32 v60, 0x3fb8aa3b, v60
	v_exp_f32_e32 v148, v60
	v_mul_f32_e32 v60, 0x3fb8aa3b, v61
	v_add_f32_e32 v65, v65, v61
	v_exp_f32_e32 v149, v60
	ds_read2_b64 v[60:63], v189 offset0:192 offset1:208
	v_and_b32_e32 v146, 0xffff0000, v146
	v_fmac_f32_e32 v146, v148, v144
	v_and_b32_e32 v144, 0xffff0000, v147
	v_fmac_f32_e32 v144, v149, v145
	s_waitcnt lgkmcnt(0)
	v_lshlrev_b32_e32 v147, 16, v61
	v_lshlrev_b32_e32 v145, 16, v60
	v_add_f32_e32 v65, v65, v147
	v_mul_f32_e32 v147, 0x3fb8aa3b, v147
	v_add_f32_e32 v64, v64, v145
	v_mul_f32_e32 v145, 0x3fb8aa3b, v145
	v_exp_f32_e32 v147, v147
	v_exp_f32_e32 v145, v145
	v_and_b32_e32 v61, 0xffff0000, v61
	v_and_b32_e32 v60, 0xffff0000, v60
	v_fmac_f32_e32 v61, v147, v144
	v_lshlrev_b32_e32 v144, 16, v62
	v_fmac_f32_e32 v60, v145, v146
	v_lshlrev_b32_e32 v145, 16, v63
	v_add_f32_e32 v64, v64, v144
	v_mul_f32_e32 v144, 0x3fb8aa3b, v144
	v_exp_f32_e32 v148, v144
	v_mul_f32_e32 v144, 0x3fb8aa3b, v145
	v_add_f32_e32 v65, v65, v145
	v_exp_f32_e32 v149, v144
	ds_read2_b64 v[144:147], v189 offset0:224 offset1:240
	v_and_b32_e32 v62, 0xffff0000, v62
	v_fmac_f32_e32 v62, v148, v60
	v_and_b32_e32 v60, 0xffff0000, v63
	v_fmac_f32_e32 v60, v149, v61
	s_waitcnt lgkmcnt(0)
	v_lshlrev_b32_e32 v63, 16, v145
	v_lshlrev_b32_e32 v61, 16, v144
	v_add_f32_e32 v65, v65, v63
	v_mul_f32_e32 v63, 0x3fb8aa3b, v63
	v_add_f32_e32 v64, v64, v61
	v_mul_f32_e32 v61, 0x3fb8aa3b, v61
	v_exp_f32_e32 v63, v63
	v_exp_f32_e32 v61, v61
	v_and_b32_e32 v145, 0xffff0000, v145
	v_and_b32_e32 v144, 0xffff0000, v144
	v_fmac_f32_e32 v145, v63, v60
	v_lshlrev_b32_e32 v60, 16, v146
	v_fmac_f32_e32 v144, v61, v62
	v_lshlrev_b32_e32 v61, 16, v147
	v_add_f32_e32 v64, v64, v60
	v_mul_f32_e32 v60, 0x3fb8aa3b, v60
	v_exp_f32_e32 v148, v60
	v_mul_f32_e32 v60, 0x3fb8aa3b, v61
	v_add_u32_e32 v150, 0x800, v189
	v_add_f32_e32 v65, v65, v61
	v_exp_f32_e32 v149, v60
	ds_read2_b64 v[60:63], v150 offset1:16
	v_and_b32_e32 v146, 0xffff0000, v146
	v_fmac_f32_e32 v146, v148, v144
	v_and_b32_e32 v144, 0xffff0000, v147
	v_fmac_f32_e32 v144, v149, v145
	s_waitcnt lgkmcnt(0)
	v_lshlrev_b32_e32 v147, 16, v61
	v_lshlrev_b32_e32 v145, 16, v60
	v_add_f32_e32 v65, v65, v147
	v_mul_f32_e32 v147, 0x3fb8aa3b, v147
	v_add_f32_e32 v64, v64, v145
	v_mul_f32_e32 v145, 0x3fb8aa3b, v145
	v_exp_f32_e32 v147, v147
	v_exp_f32_e32 v145, v145
	v_and_b32_e32 v61, 0xffff0000, v61
	v_and_b32_e32 v60, 0xffff0000, v60
	v_fmac_f32_e32 v61, v147, v144
	v_lshlrev_b32_e32 v144, 16, v62
	v_fmac_f32_e32 v60, v145, v146
	v_lshlrev_b32_e32 v145, 16, v63
	v_add_f32_e32 v64, v64, v144
	v_mul_f32_e32 v144, 0x3fb8aa3b, v144
	v_exp_f32_e32 v148, v144
	v_mul_f32_e32 v144, 0x3fb8aa3b, v145
	v_add_f32_e32 v65, v65, v145
	v_exp_f32_e32 v149, v144
	ds_read2_b64 v[144:147], v150 offset0:32 offset1:48
	v_and_b32_e32 v62, 0xffff0000, v62
	v_fmac_f32_e32 v62, v148, v60
	v_and_b32_e32 v60, 0xffff0000, v63
	v_fmac_f32_e32 v60, v149, v61
	s_waitcnt lgkmcnt(0)
	v_lshlrev_b32_e32 v63, 16, v145
	v_lshlrev_b32_e32 v61, 16, v144
	v_add_f32_e32 v65, v65, v63
	v_mul_f32_e32 v63, 0x3fb8aa3b, v63
	v_add_f32_e32 v64, v64, v61
	v_mul_f32_e32 v61, 0x3fb8aa3b, v61
	v_exp_f32_e32 v63, v63
	v_exp_f32_e32 v61, v61
	v_and_b32_e32 v145, 0xffff0000, v145
	v_and_b32_e32 v144, 0xffff0000, v144
	v_fmac_f32_e32 v145, v63, v60
	v_lshlrev_b32_e32 v60, 16, v146
	v_fmac_f32_e32 v144, v61, v62
	v_lshlrev_b32_e32 v61, 16, v147
	v_add_f32_e32 v64, v64, v60
	v_mul_f32_e32 v60, 0x3fb8aa3b, v60
	v_exp_f32_e32 v148, v60
	v_mul_f32_e32 v60, 0x3fb8aa3b, v61
	v_add_f32_e32 v65, v65, v61
	v_exp_f32_e32 v149, v60
	ds_read2_b64 v[60:63], v150 offset0:64 offset1:80
	v_and_b32_e32 v146, 0xffff0000, v146
	v_fmac_f32_e32 v146, v148, v144
	v_and_b32_e32 v144, 0xffff0000, v147
	v_fmac_f32_e32 v144, v149, v145
	s_waitcnt lgkmcnt(0)
	v_lshlrev_b32_e32 v147, 16, v61
	v_lshlrev_b32_e32 v145, 16, v60
	v_add_f32_e32 v65, v65, v147
	v_mul_f32_e32 v147, 0x3fb8aa3b, v147
	v_add_f32_e32 v64, v64, v145
	v_mul_f32_e32 v145, 0x3fb8aa3b, v145
	v_exp_f32_e32 v147, v147
	v_exp_f32_e32 v145, v145
	v_and_b32_e32 v61, 0xffff0000, v61
	v_and_b32_e32 v60, 0xffff0000, v60
	v_fmac_f32_e32 v61, v147, v144
	v_lshlrev_b32_e32 v144, 16, v62
	v_fmac_f32_e32 v60, v145, v146
	v_lshlrev_b32_e32 v145, 16, v63
	v_add_f32_e32 v64, v64, v144
	v_mul_f32_e32 v144, 0x3fb8aa3b, v144
	v_exp_f32_e32 v148, v144
	v_mul_f32_e32 v144, 0x3fb8aa3b, v145
	v_add_f32_e32 v65, v65, v145
	v_exp_f32_e32 v149, v144
	ds_read2_b64 v[144:147], v150 offset0:96 offset1:112
	v_and_b32_e32 v62, 0xffff0000, v62
	v_fmac_f32_e32 v62, v148, v60
	v_and_b32_e32 v60, 0xffff0000, v63
	v_fmac_f32_e32 v60, v149, v61
	s_waitcnt lgkmcnt(0)
	v_lshlrev_b32_e32 v63, 16, v145
	v_lshlrev_b32_e32 v61, 16, v144
	v_add_f32_e32 v65, v65, v63
	v_mul_f32_e32 v63, 0x3fb8aa3b, v63
	v_add_f32_e32 v64, v64, v61
	v_mul_f32_e32 v61, 0x3fb8aa3b, v61
	v_exp_f32_e32 v63, v63
	v_exp_f32_e32 v61, v61
	v_and_b32_e32 v145, 0xffff0000, v145
	v_and_b32_e32 v144, 0xffff0000, v144
	v_fmac_f32_e32 v145, v63, v60
	v_lshlrev_b32_e32 v60, 16, v146
	v_fmac_f32_e32 v144, v61, v62
	v_lshlrev_b32_e32 v61, 16, v147
	v_add_f32_e32 v64, v64, v60
	v_mul_f32_e32 v60, 0x3fb8aa3b, v60
	v_exp_f32_e32 v148, v60
	v_mul_f32_e32 v60, 0x3fb8aa3b, v61
	v_add_f32_e32 v65, v65, v61
	v_exp_f32_e32 v149, v60
	ds_read2_b64 v[60:63], v150 offset0:128 offset1:144
	v_and_b32_e32 v146, 0xffff0000, v146
	v_fmac_f32_e32 v146, v148, v144
	v_and_b32_e32 v144, 0xffff0000, v147
	v_fmac_f32_e32 v144, v149, v145
	s_waitcnt lgkmcnt(0)
	v_lshlrev_b32_e32 v147, 16, v61
	v_lshlrev_b32_e32 v145, 16, v60
	v_add_f32_e32 v65, v65, v147
	v_mul_f32_e32 v147, 0x3fb8aa3b, v147
	v_add_f32_e32 v64, v64, v145
	v_mul_f32_e32 v145, 0x3fb8aa3b, v145
	v_exp_f32_e32 v147, v147
	v_exp_f32_e32 v145, v145
	v_and_b32_e32 v61, 0xffff0000, v61
	v_and_b32_e32 v60, 0xffff0000, v60
	v_fmac_f32_e32 v61, v147, v144
	v_lshlrev_b32_e32 v144, 16, v62
	v_fmac_f32_e32 v60, v145, v146
	v_lshlrev_b32_e32 v145, 16, v63
	v_add_f32_e32 v64, v64, v144
	v_mul_f32_e32 v144, 0x3fb8aa3b, v144
	v_exp_f32_e32 v148, v144
	v_mul_f32_e32 v144, 0x3fb8aa3b, v145
	v_add_f32_e32 v65, v65, v145
	v_exp_f32_e32 v149, v144
	ds_read2_b64 v[144:147], v150 offset0:160 offset1:176
	v_and_b32_e32 v62, 0xffff0000, v62
	v_fmac_f32_e32 v62, v148, v60
	v_and_b32_e32 v60, 0xffff0000, v63
	v_fmac_f32_e32 v60, v149, v61
	s_waitcnt lgkmcnt(0)
	v_lshlrev_b32_e32 v63, 16, v145
	v_lshlrev_b32_e32 v61, 16, v144
	v_add_f32_e32 v65, v65, v63
	v_mul_f32_e32 v63, 0x3fb8aa3b, v63
	v_add_f32_e32 v64, v64, v61
	v_mul_f32_e32 v61, 0x3fb8aa3b, v61
	v_exp_f32_e32 v63, v63
	v_exp_f32_e32 v61, v61
	v_and_b32_e32 v145, 0xffff0000, v145
	v_and_b32_e32 v144, 0xffff0000, v144
	v_fmac_f32_e32 v145, v63, v60
	v_lshlrev_b32_e32 v60, 16, v146
	v_fmac_f32_e32 v144, v61, v62
	v_lshlrev_b32_e32 v61, 16, v147
	v_add_f32_e32 v64, v64, v60
	v_mul_f32_e32 v60, 0x3fb8aa3b, v60
	v_exp_f32_e32 v148, v60
	v_mul_f32_e32 v60, 0x3fb8aa3b, v61
	v_add_f32_e32 v65, v65, v61
	v_exp_f32_e32 v149, v60
	ds_read2_b64 v[60:63], v150 offset0:192 offset1:208
	v_and_b32_e32 v146, 0xffff0000, v146
	v_fmac_f32_e32 v146, v148, v144
	v_and_b32_e32 v144, 0xffff0000, v147
	v_fmac_f32_e32 v144, v149, v145
	s_waitcnt lgkmcnt(0)
	v_lshlrev_b32_e32 v147, 16, v61
	v_lshlrev_b32_e32 v145, 16, v60
	v_add_f32_e32 v65, v65, v147
	v_mul_f32_e32 v147, 0x3fb8aa3b, v147
	v_add_f32_e32 v64, v64, v145
	v_mul_f32_e32 v145, 0x3fb8aa3b, v145
	v_exp_f32_e32 v147, v147
	v_exp_f32_e32 v145, v145
	v_and_b32_e32 v61, 0xffff0000, v61
	v_and_b32_e32 v60, 0xffff0000, v60
	v_fmac_f32_e32 v61, v147, v144
	v_lshlrev_b32_e32 v144, 16, v62
	v_fmac_f32_e32 v60, v145, v146
	v_lshlrev_b32_e32 v145, 16, v63
	v_add_f32_e32 v64, v64, v144
	v_mul_f32_e32 v144, 0x3fb8aa3b, v144
	v_exp_f32_e32 v148, v144
	v_mul_f32_e32 v144, 0x3fb8aa3b, v145
	v_add_f32_e32 v65, v65, v145
	v_exp_f32_e32 v149, v144
	ds_read2_b64 v[144:147], v150 offset0:224 offset1:240
	v_and_b32_e32 v62, 0xffff0000, v62
	v_fmac_f32_e32 v62, v148, v60
	v_and_b32_e32 v60, 0xffff0000, v63
	v_fmac_f32_e32 v60, v149, v61
	s_waitcnt lgkmcnt(0)
	v_lshlrev_b32_e32 v61, 16, v144
	v_lshlrev_b32_e32 v63, 16, v145
	v_add_f32_e32 v64, v64, v61
	v_mul_f32_e32 v61, 0x3fb8aa3b, v61
	v_add_f32_e32 v65, v65, v63
	v_exp_f32_e32 v61, v61
	v_mul_f32_e32 v63, 0x3fb8aa3b, v63
	v_exp_f32_e32 v63, v63
	v_and_b32_e32 v144, 0xffff0000, v144
	v_fmac_f32_e32 v144, v61, v62
	v_and_b32_e32 v61, 0xffff0000, v145
	v_fmac_f32_e32 v61, v63, v60
	v_lshlrev_b32_e32 v60, 16, v146
	v_mul_f32_e32 v63, 0x3fb8aa3b, v60
	v_exp_f32_e32 v63, v63
	v_lshlrev_b32_e32 v62, 16, v147
	v_add_f32_e32 v60, v64, v60
	v_add_f32_e32 v64, v65, v62
	v_and_b32_e32 v145, 0xffff0000, v146
	v_mul_f32_e32 v62, 0x3fb8aa3b, v62
	v_mul_f32_e32 v60, 0x3fb8aa3b, v60
	v_fmac_f32_e32 v145, v63, v144
	v_exp_f32_e32 v62, v62
	v_exp_f32_e32 v144, v60
	v_mul_f32_e32 v60, 0x3fb8aa3b, v64
	v_exp_f32_e32 v146, v60
	v_and_b32_e32 v147, 0xffff0000, v147
	v_fmac_f32_e32 v147, v62, v61
	ds_bpermute_b32 v148, v73, v144
	ds_bpermute_b32 v149, v73, v146
	ds_bpermute_b32 v150, v73, v145
	ds_bpermute_b32 v151, v73, v147
	v_lshl_add_u64 v[58:59], s[46:47], 0, v[94:95]
	v_lshl_add_u64 v[62:63], s[46:47], 0, v[96:97]
	global_load_dwordx4 v[58:61], v[58:59], off nt
	s_nop 0
	global_load_dwordx4 v[62:65], v[62:63], off nt
	s_waitcnt lgkmcnt(1)
	v_fmac_f32_e32 v150, v138, v148
	s_waitcnt lgkmcnt(0)
	v_fmac_f32_e32 v151, v139, v149
	ds_bpermute_b32 v148, v166, v144
	ds_bpermute_b32 v149, v166, v145
	v_cndmask_b32_e64 v139, v151, v139, s[0:1]
	v_cndmask_b32_e64 v138, v150, v138, s[0:1]
	ds_bpermute_b32 v150, v166, v146
	ds_bpermute_b32 v151, v166, v147
	ds_bpermute_b32 v144, v167, v144
	ds_bpermute_b32 v146, v167, v146
	ds_bpermute_b32 v145, v167, v145
	ds_bpermute_b32 v147, v167, v147
	s_waitcnt lgkmcnt(6)
	v_fmac_f32_e32 v149, v138, v148
	s_waitcnt lgkmcnt(4)
	v_fmac_f32_e32 v151, v139, v150
	v_cndmask_b32_e64 v139, v139, v151, s[4:5]
	v_cndmask_b32_e64 v138, v138, v149, s[4:5]
	s_waitcnt lgkmcnt(1)
	v_fmac_f32_e32 v145, v138, v144
	s_waitcnt lgkmcnt(0)
	v_fmac_f32_e32 v147, v139, v146
	v_cndmask_b32_e64 v139, v139, v147, s[6:7]
	v_cndmask_b32_e64 v138, v138, v145, s[6:7]
	v_fmac_f32_e32 v141, v142, v138
	v_fmac_f32_e32 v140, v143, v139
	v_cvt_pk_bf16_f32 v138, v141, v140
	ds_read_b64 v[142:143], v189 offset:128
	s_cmpk_gt_i32 s53, 0x27ff
	s_waitcnt lgkmcnt(0)
	v_lshlrev_b32_e32 v139, 16, v142
	v_lshlrev_b32_e32 v144, 16, v143
	v_mul_f32_e32 v139, 0x3fb8aa3b, v139
	v_mul_f32_e32 v144, 0x3fb8aa3b, v144
	v_exp_f32_e32 v139, v139
	v_exp_f32_e32 v144, v144
	v_and_b32_e32 v142, 0xffff0000, v142
	v_and_b32_e32 v143, 0xffff0000, v143
	v_fmac_f32_e32 v142, v141, v139
	v_fmac_f32_e32 v143, v140, v144
	v_cvt_pk_bf16_f32 v139, v142, v143
	ds_read_b64 v[140:141], v189 offset:256
	s_waitcnt lgkmcnt(0)
	v_lshlrev_b32_e32 v144, 16, v140
	v_lshlrev_b32_e32 v145, 16, v141
	v_mul_f32_e32 v144, 0x3fb8aa3b, v144
	v_mul_f32_e32 v145, 0x3fb8aa3b, v145
	v_exp_f32_e32 v144, v144
	v_exp_f32_e32 v145, v145
	v_and_b32_e32 v146, 0xffff0000, v140
	v_and_b32_e32 v141, 0xffff0000, v141
	v_fmac_f32_e32 v146, v142, v144
	v_fmac_f32_e32 v141, v143, v145
	v_cvt_pk_bf16_f32 v140, v146, v141
	ds_read_b64 v[142:143], v189 offset:384
	s_waitcnt lgkmcnt(0)
	v_lshlrev_b32_e32 v144, 16, v142
	v_mul_f32_e32 v144, 0x3fb8aa3b, v144
	v_lshlrev_b32_e32 v145, 16, v143
	v_exp_f32_e32 v144, v144
	v_mul_f32_e32 v145, 0x3fb8aa3b, v145
	v_exp_f32_e32 v145, v145
	v_and_b32_e32 v147, 0xffff0000, v142
	v_fmac_f32_e32 v147, v146, v144
	v_and_b32_e32 v144, 0xffff0000, v143
	v_fmac_f32_e32 v144, v141, v145
	v_cvt_pk_bf16_f32 v141, v147, v144
	ds_read_b64 v[142:143], v189 offset:512
	s_waitcnt lgkmcnt(0)
	v_lshlrev_b32_e32 v145, 16, v142
	v_lshlrev_b32_e32 v146, 16, v143
	v_mul_f32_e32 v145, 0x3fb8aa3b, v145
	v_mul_f32_e32 v146, 0x3fb8aa3b, v146
	v_exp_f32_e32 v145, v145
	v_exp_f32_e32 v146, v146
	v_and_b32_e32 v148, 0xffff0000, v142
	v_and_b32_e32 v143, 0xffff0000, v143
	v_fmac_f32_e32 v148, v147, v145
	v_fmac_f32_e32 v143, v144, v146
	v_cvt_pk_bf16_f32 v142, v148, v143
	ds_read_b64 v[144:145], v189 offset:640
	s_waitcnt lgkmcnt(0)
	v_lshlrev_b32_e32 v146, 16, v144
	v_mul_f32_e32 v146, 0x3fb8aa3b, v146
	v_lshlrev_b32_e32 v147, 16, v145
	v_exp_f32_e32 v146, v146
	v_mul_f32_e32 v147, 0x3fb8aa3b, v147
	v_exp_f32_e32 v147, v147
	v_and_b32_e32 v149, 0xffff0000, v144
	v_fmac_f32_e32 v149, v148, v146
	v_and_b32_e32 v146, 0xffff0000, v145
	v_fmac_f32_e32 v146, v143, v147
	v_cvt_pk_bf16_f32 v143, v149, v146
	ds_read_b64 v[144:145], v189 offset:768
	s_waitcnt lgkmcnt(0)
	v_lshlrev_b32_e32 v147, 16, v144
	v_lshlrev_b32_e32 v148, 16, v145
	v_mul_f32_e32 v147, 0x3fb8aa3b, v147
	v_mul_f32_e32 v148, 0x3fb8aa3b, v148
	v_exp_f32_e32 v147, v147
	v_exp_f32_e32 v148, v148
	v_and_b32_e32 v150, 0xffff0000, v144
	v_and_b32_e32 v145, 0xffff0000, v145
	v_fmac_f32_e32 v150, v149, v147
	v_fmac_f32_e32 v145, v146, v148
	v_cvt_pk_bf16_f32 v144, v150, v145
	ds_read_b64 v[146:147], v189 offset:896
	s_waitcnt lgkmcnt(0)
	v_lshlrev_b32_e32 v148, 16, v146
	v_lshlrev_b32_e32 v149, 16, v147
	v_mul_f32_e32 v148, 0x3fb8aa3b, v148
	v_mul_f32_e32 v149, 0x3fb8aa3b, v149
	v_exp_f32_e32 v148, v148
	v_exp_f32_e32 v149, v149
	v_and_b32_e32 v151, 0xffff0000, v146
	v_and_b32_e32 v147, 0xffff0000, v147
	v_fmac_f32_e32 v151, v150, v148
	v_fmac_f32_e32 v147, v145, v149
	v_cvt_pk_bf16_f32 v146, v151, v147
	ds_read_b64 v[148:149], v189 offset:1024
	s_waitcnt lgkmcnt(0)
	v_lshlrev_b32_e32 v145, 16, v148
	v_mul_f32_e32 v145, 0x3fb8aa3b, v145
	v_lshlrev_b32_e32 v150, 16, v149
	v_exp_f32_e32 v145, v145
	v_mul_f32_e32 v150, 0x3fb8aa3b, v150
	v_exp_f32_e32 v150, v150
	v_and_b32_e32 v152, 0xffff0000, v148
	v_fmac_f32_e32 v152, v151, v145
	v_and_b32_e32 v145, 0xffff0000, v149
	v_fmac_f32_e32 v145, v147, v150
	v_cvt_pk_bf16_f32 v148, v152, v145
	ds_read_b64 v[150:151], v189 offset:1152
	s_waitcnt lgkmcnt(0)
	v_lshlrev_b32_e32 v147, 16, v150
	v_mul_f32_e32 v147, 0x3fb8aa3b, v147
	v_lshlrev_b32_e32 v149, 16, v151
	v_exp_f32_e32 v147, v147
	v_mul_f32_e32 v149, 0x3fb8aa3b, v149
	v_exp_f32_e32 v149, v149
	v_and_b32_e32 v154, 0xffff0000, v150
	v_fmac_f32_e32 v154, v152, v147
	v_and_b32_e32 v147, 0xffff0000, v151
	v_fmac_f32_e32 v147, v145, v149
	v_cvt_pk_bf16_f32 v150, v154, v147
	ds_read_b64 v[152:153], v189 offset:1280
	s_waitcnt lgkmcnt(0)
	v_lshlrev_b32_e32 v145, 16, v152
	v_mul_f32_e32 v145, 0x3fb8aa3b, v145
	v_lshlrev_b32_e32 v149, 16, v153
	v_exp_f32_e32 v145, v145
	v_mul_f32_e32 v149, 0x3fb8aa3b, v149
	v_exp_f32_e32 v149, v149
	v_and_b32_e32 v151, 0xffff0000, v152
	v_fmac_f32_e32 v151, v154, v145
	v_and_b32_e32 v145, 0xffff0000, v153
	v_fmac_f32_e32 v145, v147, v149
	v_cvt_pk_bf16_f32 v152, v151, v145
	ds_read_b64 v[154:155], v189 offset:1408
	s_waitcnt lgkmcnt(0)
	v_lshlrev_b32_e32 v147, 16, v154
	v_mul_f32_e32 v147, 0x3fb8aa3b, v147
	v_lshlrev_b32_e32 v149, 16, v155
	v_exp_f32_e32 v147, v147
	v_mul_f32_e32 v149, 0x3fb8aa3b, v149
	v_exp_f32_e32 v149, v149
	v_and_b32_e32 v153, 0xffff0000, v154
	v_fmac_f32_e32 v153, v151, v147
	v_and_b32_e32 v147, 0xffff0000, v155
	v_fmac_f32_e32 v147, v145, v149
	v_cvt_pk_bf16_f32 v155, v153, v147
	ds_read_b64 v[156:157], v189 offset:1536
	s_waitcnt lgkmcnt(0)
	v_lshlrev_b32_e32 v145, 16, v156
	v_mul_f32_e32 v145, 0x3fb8aa3b, v145
	v_lshlrev_b32_e32 v149, 16, v157
	v_exp_f32_e32 v145, v145
	v_mul_f32_e32 v149, 0x3fb8aa3b, v149
	v_exp_f32_e32 v149, v149
	v_and_b32_e32 v151, 0xffff0000, v156
	v_fmac_f32_e32 v151, v153, v145
	v_and_b32_e32 v145, 0xffff0000, v157
	v_fmac_f32_e32 v145, v147, v149
	v_cvt_pk_bf16_f32 v157, v151, v145
	ds_read_b64 v[194:195], v189 offset:1664
	s_waitcnt lgkmcnt(0)
	v_lshlrev_b32_e32 v147, 16, v194
	v_mul_f32_e32 v147, 0x3fb8aa3b, v147
	v_lshlrev_b32_e32 v149, 16, v195
	v_exp_f32_e32 v147, v147
	v_mul_f32_e32 v149, 0x3fb8aa3b, v149
	v_exp_f32_e32 v149, v149
	v_and_b32_e32 v153, 0xffff0000, v194
	v_fmac_f32_e32 v153, v151, v147
	v_and_b32_e32 v147, 0xffff0000, v195
	v_fmac_f32_e32 v147, v145, v149
	v_cvt_pk_bf16_f32 v194, v153, v147
	ds_read_b64 v[196:197], v189 offset:1792
	s_waitcnt lgkmcnt(0)
	v_lshlrev_b32_e32 v145, 16, v196
	v_mul_f32_e32 v145, 0x3fb8aa3b, v145
	v_lshlrev_b32_e32 v149, 16, v197
	v_exp_f32_e32 v145, v145
	v_mul_f32_e32 v149, 0x3fb8aa3b, v149
	v_exp_f32_e32 v149, v149
	v_and_b32_e32 v151, 0xffff0000, v196
	v_fmac_f32_e32 v151, v153, v145
	v_and_b32_e32 v145, 0xffff0000, v197
	v_fmac_f32_e32 v145, v147, v149
	v_cvt_pk_bf16_f32 v196, v151, v145
	ds_read_b64 v[198:199], v189 offset:1920
	s_waitcnt lgkmcnt(0)
	v_lshlrev_b32_e32 v147, 16, v198
	v_mul_f32_e32 v147, 0x3fb8aa3b, v147
	v_lshlrev_b32_e32 v149, 16, v199
	v_exp_f32_e32 v147, v147
	v_mul_f32_e32 v149, 0x3fb8aa3b, v149
	v_exp_f32_e32 v149, v149
	v_and_b32_e32 v153, 0xffff0000, v198
	v_fmac_f32_e32 v153, v151, v147
	v_and_b32_e32 v147, 0xffff0000, v199
	v_fmac_f32_e32 v147, v145, v149
	v_cvt_pk_bf16_f32 v198, v153, v147
	ds_read_b64 v[200:201], v189 offset:2048
	s_waitcnt lgkmcnt(0)
	v_lshlrev_b32_e32 v145, 16, v200
	v_mul_f32_e32 v145, 0x3fb8aa3b, v145
	v_lshlrev_b32_e32 v149, 16, v201
	v_exp_f32_e32 v145, v145
	v_mul_f32_e32 v149, 0x3fb8aa3b, v149
	v_exp_f32_e32 v149, v149
	v_and_b32_e32 v151, 0xffff0000, v200
	v_fmac_f32_e32 v151, v153, v145
	v_and_b32_e32 v145, 0xffff0000, v201
	v_fmac_f32_e32 v145, v147, v149
	v_cvt_pk_bf16_f32 v201, v151, v145
	ds_read_b64 v[202:203], v189 offset:2176
	s_waitcnt lgkmcnt(0)
	v_lshlrev_b32_e32 v147, 16, v202
	v_mul_f32_e32 v147, 0x3fb8aa3b, v147
	v_lshlrev_b32_e32 v149, 16, v203
	v_exp_f32_e32 v147, v147
	v_mul_f32_e32 v149, 0x3fb8aa3b, v149
	v_exp_f32_e32 v149, v149
	v_and_b32_e32 v153, 0xffff0000, v202
	v_fmac_f32_e32 v153, v151, v147
	v_and_b32_e32 v147, 0xffff0000, v203
	v_fmac_f32_e32 v147, v145, v149
	v_cvt_pk_bf16_f32 v203, v153, v147
	ds_read_b64 v[204:205], v189 offset:2304
	s_waitcnt lgkmcnt(0)
	v_lshlrev_b32_e32 v145, 16, v204
	v_mul_f32_e32 v145, 0x3fb8aa3b, v145
	v_lshlrev_b32_e32 v149, 16, v205
	v_exp_f32_e32 v145, v145
	v_mul_f32_e32 v149, 0x3fb8aa3b, v149
	v_exp_f32_e32 v149, v149
	v_and_b32_e32 v151, 0xffff0000, v204
	v_fmac_f32_e32 v151, v153, v145
	v_and_b32_e32 v145, 0xffff0000, v205
	v_fmac_f32_e32 v145, v147, v149
	v_cvt_pk_bf16_f32 v205, v151, v145
	ds_read_b64 v[206:207], v189 offset:2432
	s_waitcnt lgkmcnt(0)
	v_lshlrev_b32_e32 v147, 16, v206
	v_mul_f32_e32 v147, 0x3fb8aa3b, v147
	v_lshlrev_b32_e32 v149, 16, v207
	v_exp_f32_e32 v147, v147
	v_mul_f32_e32 v149, 0x3fb8aa3b, v149
	v_exp_f32_e32 v149, v149
	v_and_b32_e32 v153, 0xffff0000, v206
	v_fmac_f32_e32 v153, v151, v147
	v_and_b32_e32 v147, 0xffff0000, v207
	v_fmac_f32_e32 v147, v145, v149
	v_cvt_pk_bf16_f32 v207, v153, v147
	ds_read_b64 v[208:209], v189 offset:2560
	s_waitcnt lgkmcnt(0)
	v_lshlrev_b32_e32 v145, 16, v208
	v_mul_f32_e32 v145, 0x3fb8aa3b, v145
	v_lshlrev_b32_e32 v149, 16, v209
	v_exp_f32_e32 v145, v145
	v_mul_f32_e32 v149, 0x3fb8aa3b, v149
	v_exp_f32_e32 v149, v149
	v_and_b32_e32 v151, 0xffff0000, v208
	v_fmac_f32_e32 v151, v153, v145
	v_and_b32_e32 v145, 0xffff0000, v209
	v_fmac_f32_e32 v145, v147, v149
	v_cvt_pk_bf16_f32 v209, v151, v145
	ds_read_b64 v[210:211], v189 offset:2688
	s_waitcnt lgkmcnt(0)
	v_lshlrev_b32_e32 v147, 16, v210
	v_mul_f32_e32 v147, 0x3fb8aa3b, v147
	v_lshlrev_b32_e32 v149, 16, v211
	v_exp_f32_e32 v147, v147
	v_mul_f32_e32 v149, 0x3fb8aa3b, v149
	v_exp_f32_e32 v149, v149
	v_and_b32_e32 v153, 0xffff0000, v210
	v_fmac_f32_e32 v153, v151, v147
	v_and_b32_e32 v147, 0xffff0000, v211
	v_fmac_f32_e32 v147, v145, v149
	v_cvt_pk_bf16_f32 v211, v153, v147
	ds_read_b64 v[212:213], v189 offset:2816
	s_waitcnt lgkmcnt(0)
	v_lshlrev_b32_e32 v145, 16, v212
	v_mul_f32_e32 v145, 0x3fb8aa3b, v145
	v_lshlrev_b32_e32 v149, 16, v213
	v_exp_f32_e32 v145, v145
	v_mul_f32_e32 v149, 0x3fb8aa3b, v149
	v_exp_f32_e32 v149, v149
	v_and_b32_e32 v151, 0xffff0000, v212
	v_fmac_f32_e32 v151, v153, v145
	v_and_b32_e32 v145, 0xffff0000, v213
	v_fmac_f32_e32 v145, v147, v149
	v_cvt_pk_bf16_f32 v214, v151, v145
	ds_read_b64 v[212:213], v189 offset:2944
	s_waitcnt lgkmcnt(0)
	v_lshlrev_b32_e32 v147, 16, v212
	v_mul_f32_e32 v147, 0x3fb8aa3b, v147
	v_lshlrev_b32_e32 v149, 16, v213
	v_exp_f32_e32 v147, v147
	v_mul_f32_e32 v149, 0x3fb8aa3b, v149
	v_exp_f32_e32 v149, v149
	v_and_b32_e32 v153, 0xffff0000, v212
	v_fmac_f32_e32 v153, v151, v147
	v_and_b32_e32 v147, 0xffff0000, v213
	v_fmac_f32_e32 v147, v145, v149
	v_cvt_pk_bf16_f32 v216, v153, v147
	ds_read_b64 v[212:213], v189 offset:3072
	s_waitcnt lgkmcnt(0)
	v_lshlrev_b32_e32 v145, 16, v212
	v_mul_f32_e32 v145, 0x3fb8aa3b, v145
	v_lshlrev_b32_e32 v149, 16, v213
	v_exp_f32_e32 v145, v145
	v_mul_f32_e32 v149, 0x3fb8aa3b, v149
	v_exp_f32_e32 v149, v149
	v_and_b32_e32 v151, 0xffff0000, v212
	v_fmac_f32_e32 v151, v153, v145
	v_and_b32_e32 v145, 0xffff0000, v213
	v_fmac_f32_e32 v145, v147, v149
	v_cvt_pk_bf16_f32 v218, v151, v145
	ds_read_b64 v[212:213], v189 offset:3200
	s_waitcnt lgkmcnt(0)
	v_lshlrev_b32_e32 v147, 16, v212
	v_mul_f32_e32 v147, 0x3fb8aa3b, v147
	v_lshlrev_b32_e32 v149, 16, v213
	v_exp_f32_e32 v147, v147
	v_mul_f32_e32 v149, 0x3fb8aa3b, v149
	v_exp_f32_e32 v149, v149
	v_and_b32_e32 v153, 0xffff0000, v212
	v_fmac_f32_e32 v153, v151, v147
	v_and_b32_e32 v147, 0xffff0000, v213
	v_fmac_f32_e32 v147, v145, v149
	v_cvt_pk_bf16_f32 v220, v153, v147
	ds_read_b64 v[212:213], v189 offset:3328
	s_waitcnt lgkmcnt(0)
	v_lshlrev_b32_e32 v145, 16, v212
	v_mul_f32_e32 v145, 0x3fb8aa3b, v145
	v_lshlrev_b32_e32 v149, 16, v213
	v_exp_f32_e32 v145, v145
	v_mul_f32_e32 v149, 0x3fb8aa3b, v149
	v_exp_f32_e32 v149, v149
	v_and_b32_e32 v151, 0xffff0000, v212
	v_fmac_f32_e32 v151, v153, v145
	v_and_b32_e32 v145, 0xffff0000, v213
	v_fmac_f32_e32 v145, v147, v149
	v_cvt_pk_bf16_f32 v222, v151, v145
	ds_read_b64 v[212:213], v189 offset:3456
	s_waitcnt lgkmcnt(0)
	v_lshlrev_b32_e32 v147, 16, v212
	v_mul_f32_e32 v147, 0x3fb8aa3b, v147
	v_lshlrev_b32_e32 v149, 16, v213
	v_exp_f32_e32 v147, v147
	v_mul_f32_e32 v149, 0x3fb8aa3b, v149
	v_exp_f32_e32 v149, v149
	v_and_b32_e32 v153, 0xffff0000, v212
	v_fmac_f32_e32 v153, v151, v147
	v_and_b32_e32 v147, 0xffff0000, v213
	v_fmac_f32_e32 v147, v145, v149
	v_cvt_pk_bf16_f32 v225, v153, v147
	ds_read_b64 v[212:213], v189 offset:3584
	s_waitcnt lgkmcnt(0)
	v_lshlrev_b32_e32 v145, 16, v212
	v_mul_f32_e32 v145, 0x3fb8aa3b, v145
	v_lshlrev_b32_e32 v149, 16, v213
	v_exp_f32_e32 v145, v145
	v_mul_f32_e32 v149, 0x3fb8aa3b, v149
	v_exp_f32_e32 v149, v149
	v_and_b32_e32 v151, 0xffff0000, v212
	v_fmac_f32_e32 v151, v153, v145
	v_and_b32_e32 v145, 0xffff0000, v213
	v_fmac_f32_e32 v145, v147, v149
	v_cvt_pk_bf16_f32 v227, v151, v145
	ds_read_b64 v[212:213], v189 offset:3712
	s_waitcnt lgkmcnt(0)
	v_lshlrev_b32_e32 v147, 16, v212
	v_mul_f32_e32 v147, 0x3fb8aa3b, v147
	v_lshlrev_b32_e32 v149, 16, v213
	v_exp_f32_e32 v147, v147
	v_mul_f32_e32 v149, 0x3fb8aa3b, v149
	v_exp_f32_e32 v149, v149
	v_and_b32_e32 v153, 0xffff0000, v212
	v_fmac_f32_e32 v153, v151, v147
	v_and_b32_e32 v147, 0xffff0000, v213
	v_fmac_f32_e32 v147, v145, v149
	v_cvt_pk_bf16_f32 v229, v153, v147
	ds_read_b64 v[212:213], v189 offset:3840
	s_waitcnt lgkmcnt(0)
	v_lshlrev_b32_e32 v145, 16, v212
	v_mul_f32_e32 v145, 0x3fb8aa3b, v145
	v_lshlrev_b32_e32 v149, 16, v213
	v_exp_f32_e32 v145, v145
	v_mul_f32_e32 v149, 0x3fb8aa3b, v149
	v_exp_f32_e32 v149, v149
	v_and_b32_e32 v151, 0xffff0000, v212
	v_fmac_f32_e32 v151, v153, v145
	v_and_b32_e32 v145, 0xffff0000, v213
	v_fmac_f32_e32 v145, v147, v149
	v_cvt_pk_bf16_f32 v231, v151, v145
	ds_read_b64 v[212:213], v189 offset:3968
	s_waitcnt lgkmcnt(0)
	v_lshlrev_b32_e32 v147, 16, v212
	v_mul_f32_e32 v147, 0x3fb8aa3b, v147
	v_lshlrev_b32_e32 v149, 16, v213
	v_exp_f32_e32 v147, v147
	v_mul_f32_e32 v149, 0x3fb8aa3b, v149
	v_exp_f32_e32 v149, v149
	v_and_b32_e32 v153, 0xffff0000, v212
	v_fmac_f32_e32 v153, v151, v147
	v_and_b32_e32 v147, 0xffff0000, v213
	v_fmac_f32_e32 v147, v145, v149
	v_or_b32_e32 v145, s44, v68
	v_mov_b64_e32 v[212:213], s[12:13]
	v_mad_u64_u32 v[212:213], s[46:47], v145, s3, v[212:213]
	v_mad_i32_i24 v213, s45, v169, v213
	v_lshl_add_u64 v[100:101], v[100:101], 1, v[212:213]
	v_cvt_pk_bf16_f32 v233, v153, v147
	global_load_dword v145, v[100:101], off
	v_lshl_add_u64 v[100:101], v[100:101], 0, s[38:39]
	global_load_dword v147, v[100:101], off
	v_lshl_add_u64 v[100:101], v[100:101], 0, s[38:39]
	global_load_dword v149, v[100:101], off
	v_lshl_add_u64 v[100:101], v[100:101], 0, s[38:39]
	global_load_dword v151, v[100:101], off
	v_lshl_add_u64 v[100:101], v[100:101], 0, s[38:39]
	global_load_dword v153, v[100:101], off
	v_lshl_add_u64 v[100:101], v[100:101], 0, s[38:39]
	global_load_dword v154, v[100:101], off
	v_lshl_add_u64 v[100:101], v[100:101], 0, s[38:39]
	global_load_dword v156, v[100:101], off
	v_lshl_add_u64 v[100:101], v[100:101], 0, s[38:39]
	global_load_dword v193, v[100:101], off
	v_lshl_add_u64 v[100:101], v[100:101], 0, s[38:39]
	global_load_dword v195, v[100:101], off
	v_lshl_add_u64 v[100:101], v[100:101], 0, s[38:39]
	global_load_dword v197, v[100:101], off
	v_lshl_add_u64 v[100:101], v[100:101], 0, s[38:39]
	global_load_dword v199, v[100:101], off
	v_lshl_add_u64 v[100:101], v[100:101], 0, s[38:39]
	global_load_dword v200, v[100:101], off
	v_lshl_add_u64 v[100:101], v[100:101], 0, s[38:39]
	global_load_dword v202, v[100:101], off
	v_lshl_add_u64 v[100:101], v[100:101], 0, s[38:39]
	global_load_dword v204, v[100:101], off
	v_lshl_add_u64 v[100:101], v[100:101], 0, s[38:39]
	global_load_dword v206, v[100:101], off
	v_lshl_add_u64 v[100:101], v[100:101], 0, s[38:39]
	global_load_dword v208, v[100:101], off
	v_lshl_add_u64 v[100:101], v[100:101], 0, s[38:39]
	global_load_dword v210, v[100:101], off
	v_lshl_add_u64 v[100:101], v[100:101], 0, s[38:39]
	global_load_dword v212, v[100:101], off
	v_lshl_add_u64 v[100:101], v[100:101], 0, s[38:39]
	global_load_dword v213, v[100:101], off
	v_lshl_add_u64 v[100:101], v[100:101], 0, s[38:39]
	global_load_dword v215, v[100:101], off
	v_lshl_add_u64 v[100:101], v[100:101], 0, s[38:39]
	global_load_dword v217, v[100:101], off
	v_lshl_add_u64 v[100:101], v[100:101], 0, s[38:39]
	global_load_dword v219, v[100:101], off
	v_lshl_add_u64 v[100:101], v[100:101], 0, s[38:39]
	global_load_dword v221, v[100:101], off
	v_lshl_add_u64 v[100:101], v[100:101], 0, s[38:39]
	global_load_dword v223, v[100:101], off
	v_lshl_add_u64 v[100:101], v[100:101], 0, s[38:39]
	global_load_dword v224, v[100:101], off
	v_lshl_add_u64 v[100:101], v[100:101], 0, s[38:39]
	global_load_dword v226, v[100:101], off
	v_lshl_add_u64 v[100:101], v[100:101], 0, s[38:39]
	global_load_dword v228, v[100:101], off
	v_lshl_add_u64 v[100:101], v[100:101], 0, s[38:39]
	global_load_dword v230, v[100:101], off
	v_lshl_add_u64 v[100:101], v[100:101], 0, s[38:39]
	global_load_dword v232, v[100:101], off
	v_lshl_add_u64 v[100:101], v[100:101], 0, s[38:39]
	global_load_dword v234, v[100:101], off
	v_lshl_add_u64 v[100:101], v[100:101], 0, s[38:39]
	global_load_dword v235, v[100:101], off
	v_lshl_add_u64 v[100:101], v[100:101], 0, s[38:39]
	global_load_dword v236, v[100:101], off
	s_waitcnt vmcnt(32)
	v_pk_fma_f32 v[100:101], v[102:103], 0, v[106:107] op_sel_hi:[1,0,1]
	v_pk_mul_f32 v[102:103], v[102:103], v[110:111]
	v_pk_fma_f32 v[100:101], v[100:101], v[110:111], v[104:105]
	v_pk_mul_f32 v[102:103], v[102:103], v[108:109]
	v_pk_fma_f32 v[100:101], v[100:101], v[108:109], v[114:115]
	v_pk_mul_f32 v[102:103], v[102:103], v[118:119]
	v_pk_fma_f32 v[100:101], v[100:101], v[118:119], v[112:113]
	v_pk_mul_f32 v[102:103], v[102:103], v[116:117]
	v_pk_fma_f32 v[100:101], v[100:101], v[116:117], v[122:123]
	v_pk_mul_f32 v[102:103], v[102:103], v[126:127]
	v_pk_fma_f32 v[100:101], v[100:101], v[126:127], v[120:121]
	v_pk_mul_f32 v[102:103], v[102:103], v[124:125]
	v_pk_fma_f32 v[100:101], v[100:101], v[124:125], v[130:131]
	v_pk_mul_f32 v[102:103], v[102:103], v[134:135]
	v_pk_fma_f32 v[100:101], v[100:101], v[134:135], v[128:129]
	v_pk_mul_f32 v[108:109], v[102:103], v[132:133]
	v_pk_fma_f32 v[110:111], v[100:101], v[132:133], v[136:137]
	ds_bpermute_b32 v112, v73, v108
	ds_bpermute_b32 v113, v73, v109
	ds_bpermute_b32 v114, v73, v110
	ds_bpermute_b32 v115, v73, v111
	ds_bpermute_b32 v100, v166, v108
	ds_bpermute_b32 v101, v166, v109
	ds_bpermute_b32 v102, v166, v110
	ds_bpermute_b32 v103, v166, v111
	ds_bpermute_b32 v104, v167, v108
	ds_bpermute_b32 v105, v167, v109
	ds_bpermute_b32 v106, v167, v110
	ds_bpermute_b32 v107, v167, v111
	ds_bpermute_b32 v108, v168, v108
	ds_bpermute_b32 v109, v168, v109
	ds_bpermute_b32 v110, v168, v110
	ds_bpermute_b32 v111, v168, v111
	s_cselect_b64 s[46:47], -1, 0
	s_and_b64 vcc, exec, s[46:47]
	ds_write_b128 v173, v[22:25]
	ds_write_b128 v174, v[2:5]
	ds_write_b128 v175, v[6:9]
	ds_write_b128 v176, v[10:13]
	ds_write_b128 v177, v[14:17] offset:128
	ds_write_b128 v178, v[18:21] offset:128
	ds_write_b128 v179, v[26:29] offset:128
	ds_write_b128 v180, v[30:33] offset:128
	ds_write_b128 v181, v[34:37] offset:256
	ds_write_b128 v182, v[38:41] offset:256
	ds_write_b128 v183, v[42:45] offset:256
	ds_write_b128 v184, v[46:49] offset:256
	ds_write_b128 v185, v[50:53] offset:384
	ds_write_b128 v186, v[54:57] offset:384
	ds_write_b128 v187, v[58:61] offset:384
	ds_write_b128 v188, v[62:65] offset:384
	s_cbranch_vccnz .Lp9_nonext
	s_ashr_i32 s48, s53, 2
	s_ashr_i32 s49, s48, 31
	s_lshl_b64 s[48:49], s[48:49], 17
	s_add_u32 s43, s29, s48
	s_addc_u32 s49, s30, s49
	s_and_b32 s48, s34, 0xc000
	s_add_u32 s48, s43, s48
	s_addc_u32 s49, s49, 0
	v_lshl_add_u64 v[10:11], s[48:49], 0, v[66:67]
	global_load_dwordx4 v[22:25], v[10:11], off nt
	global_load_dwordx4 v[2:5], v[10:11], off offset:1024 nt
	global_load_dwordx4 v[6:9], v[10:11], off offset:2048 nt
	s_nop 0
	global_load_dwordx4 v[10:13], v[10:11], off offset:3072 nt
	v_lshl_add_u64 v[14:15], s[48:49], 0, v[74:75]
	v_lshl_add_u64 v[18:19], s[48:49], 0, v[76:77]
	v_lshl_add_u64 v[26:27], s[48:49], 0, v[78:79]
	v_lshl_add_u64 v[30:31], s[48:49], 0, v[80:81]
	v_lshl_add_u64 v[34:35], s[48:49], 0, v[82:83]
	v_lshl_add_u64 v[38:39], s[48:49], 0, v[84:85]
	v_lshl_add_u64 v[42:43], s[48:49], 0, v[86:87]
	v_lshl_add_u64 v[46:47], s[48:49], 0, v[88:89]
	v_lshl_add_u64 v[50:51], s[48:49], 0, v[90:91]
	v_lshl_add_u64 v[54:55], s[48:49], 0, v[92:93]
	v_lshl_add_u64 v[58:59], s[48:49], 0, v[94:95]
	v_lshl_add_u64 v[62:63], s[48:49], 0, v[96:97]
	global_load_dwordx4 v[14:17], v[14:15], off nt
	s_nop 0
	global_load_dwordx4 v[18:21], v[18:19], off nt
	s_nop 0
	global_load_dwordx4 v[26:29], v[26:27], off nt
	s_nop 0
	global_load_dwordx4 v[30:33], v[30:31], off nt
	s_nop 0
	global_load_dwordx4 v[34:37], v[34:35], off nt
	s_nop 0
	global_load_dwordx4 v[38:41], v[38:39], off nt
	s_nop 0
	global_load_dwordx4 v[42:45], v[42:43], off nt
	s_nop 0
	global_load_dwordx4 v[46:49], v[46:47], off nt
	s_nop 0
	global_load_dwordx4 v[50:53], v[50:51], off nt
	s_nop 0
	global_load_dwordx4 v[54:57], v[54:55], off nt
	s_nop 0
	global_load_dwordx4 v[58:61], v[58:59], off nt
	s_nop 0
	global_load_dwordx4 v[62:65], v[62:63], off nt
	s_branch .LBB0_1466
.Lp9_nonext:
	s_waitcnt vmcnt(0)
	s_branch .LBB0_1466
